# phase 8 unit transition: next unit's accumulator-init bias loads hoisted to the start of the epilogue (ahead of its 8 write-through stores), wait before acc init vmcnt(0) -> vmcnt(8)
# speedup vs baseline: 1.0037x; 1.0031x over previous
.LBB0_1232:
	s_and_b64 vcc, exec, s[8:9]
	s_cbranch_vccnz .Lbh_skip_a
	v_readlane_b32 s100, v254, 8
	v_readlane_b32 s101, v254, 9
	s_lshl_b32 s98, s48, 14
	v_mbcnt_lo_u32_b32 v156, -1, 0
	s_add_u32 s100, s100, s98
	s_addc_u32 s101, s101, 0
	s_lshl_b32 s98, s50, 9
	v_mbcnt_hi_u32_b32 v156, -1, v156
	s_add_u32 s100, s100, s98
	s_addc_u32 s101, s101, 0
	s_lshl_b32 s98, s5, 2
	v_ashrrev_i32_e32 v156, 1, v156
	s_add_u32 s100, s100, s98
	s_addc_u32 s101, s101, 0
	v_and_b32_e32 v156, -8, v156
	v_ashrrev_i32_e32 v157, 31, v156
	v_lshl_add_u64 v[156:157], v[156:157], 2, s[100:101]
	s_movk_i32 s100, 0x2000
	s_mov_b32 s101, 0
	v_lshl_add_u64 v[158:159], v[156:157], 0, s[18:19]
	global_load_dwordx4 v[148:151], v[156:157], off offset:16
	global_load_dwordx4 v[140:143], v[156:157], off
	v_lshl_add_u64 v[156:157], v[156:157], 0, s[100:101]
	global_load_dwordx4 v[152:155], v[158:159], off offset:16
	global_load_dwordx4 v[144:147], v[156:157], off
.Lbh_skip_a:
	s_add_u32 s58, s2, 0xffffff00
	s_addc_u32 s59, s49, -1
	s_lshl_b32 s2, s43, 2
	s_add_i32 s2, s2, 0
	s_add_i32 s2, s2, 0x24080
	v_mov_b32_e32 v42, v131
	v_mov_b32_e32 v43, s2
	ds_read_b32 v43, v43
	v_mbcnt_lo_u32_b32 v42, -1, v42
	s_lshl_b32 s2, s69, 8
	v_mbcnt_hi_u32_b32 v42, -1, v42
	s_add_i32 s2, s2, s78
	v_ashrrev_i32_e32 v44, 1, v42
	v_and_or_b32 v42, v42, 15, s2
	s_lshl_b32 s34, s26, 7
	s_waitcnt lgkmcnt(0)
	v_add_u32_e32 v136, v42, v43
	v_max_f32_e32 v42, v94, v94
	v_and_b32_e32 v44, -8, v44
	s_or_b32 s34, s34, s5
	v_min_f32_e32 v42, 0x44e00000, v42
	v_add_u32_e32 v134, s34, v44
	v_mul_f32_e32 v44, 0x37800000, v42
	v_mul_f32_e32 v42, 0xbc1d265f, v42
	v_exp_f32_e32 v42, v42
	v_med3_f32 v43, v62, s82, v139
	v_add_f32_e32 v43, 0x43800000, v43
	v_ashrrev_i32_e32 v137, 31, v136
	v_add_f32_e32 v42, 1.0, v42
	v_rcp_f32_e32 v42, v42
	v_ashrrev_i32_e32 v135, 31, v134
	s_mov_b64 s[34:35], 0x8000
	s_and_b64 vcc, exec, s[8:9]
	v_mul_f32_e32 v42, v44, v42
	v_mul_f32_e32 v43, v42, v43
	v_max_f32_e32 v42, v90, v90
	v_min_f32_e32 v42, 0x44e00000, v42
	v_mul_f32_e32 v45, 0x37800000, v42
	v_mul_f32_e32 v42, 0xbc1d265f, v42
	v_exp_f32_e32 v42, v42
	v_med3_f32 v44, v58, s82, v139
	v_add_f32_e32 v44, 0x43800000, v44
	v_add_f32_e32 v42, 1.0, v42
	v_rcp_f32_e32 v42, v42
	s_nop 0
	v_mul_f32_e32 v42, v45, v42
	v_mul_f32_e32 v44, v42, v44
	v_max_f32_e32 v42, v95, v95
	v_min_f32_e32 v42, 0x44e00000, v42
	v_mul_f32_e32 v46, 0x37800000, v42
	v_mul_f32_e32 v42, 0xbc1d265f, v42
	v_exp_f32_e32 v42, v42
	v_med3_f32 v45, v63, s82, v139
	v_add_f32_e32 v45, 0x43800000, v45
	v_add_f32_e32 v42, 1.0, v42
	v_rcp_f32_e32 v42, v42
	s_nop 0
	v_mul_f32_e32 v42, v46, v42
	v_mul_f32_e32 v45, v42, v45
	v_max_f32_e32 v42, v91, v91
	v_min_f32_e32 v42, 0x44e00000, v42
	v_mul_f32_e32 v47, 0x37800000, v42
	v_mul_f32_e32 v42, 0xbc1d265f, v42
	v_exp_f32_e32 v42, v42
	v_med3_f32 v46, v59, s82, v139
	v_add_f32_e32 v46, 0x43800000, v46
	v_add_f32_e32 v42, 1.0, v42
	v_rcp_f32_e32 v42, v42
	s_nop 0
	v_mul_f32_e32 v42, v47, v42
	v_mul_f32_e32 v46, v42, v46
	v_max_f32_e32 v42, v96, v96
	v_min_f32_e32 v42, 0x44e00000, v42
	v_mul_f32_e32 v48, 0x37800000, v42
	v_mul_f32_e32 v42, 0xbc1d265f, v42
	v_exp_f32_e32 v42, v42
	v_med3_f32 v47, v64, s82, v139
	v_add_f32_e32 v47, 0x43800000, v47
	v_add_f32_e32 v42, 1.0, v42
	v_rcp_f32_e32 v42, v42
	s_nop 0
	v_mul_f32_e32 v42, v48, v42
	v_mul_f32_e32 v47, v42, v47
	v_max_f32_e32 v42, v92, v92
	v_min_f32_e32 v42, 0x44e00000, v42
	v_mul_f32_e32 v49, 0x37800000, v42
	v_mul_f32_e32 v42, 0xbc1d265f, v42
	v_exp_f32_e32 v42, v42
	v_med3_f32 v48, v60, s82, v139
	v_add_f32_e32 v48, 0x43800000, v48
	v_add_f32_e32 v42, 1.0, v42
	v_rcp_f32_e32 v42, v42
	s_nop 0
	v_mul_f32_e32 v42, v49, v42
	v_mul_f32_e32 v48, v42, v48
	v_max_f32_e32 v42, v97, v97
	v_min_f32_e32 v42, 0x44e00000, v42
	v_mul_f32_e32 v50, 0x37800000, v42
	v_mul_f32_e32 v42, 0xbc1d265f, v42
	v_exp_f32_e32 v42, v42
	v_med3_f32 v49, v65, s82, v139
	v_add_f32_e32 v49, 0x43800000, v49
	v_add_f32_e32 v42, 1.0, v42
	v_rcp_f32_e32 v42, v42
	s_nop 0
	v_mul_f32_e32 v42, v50, v42
	v_mul_f32_e32 v49, v42, v49
	v_max_f32_e32 v42, v93, v93
	v_min_f32_e32 v42, 0x44e00000, v42
	v_mul_f32_e32 v51, 0x37800000, v42
	v_mul_f32_e32 v42, 0xbc1d265f, v42
	v_exp_f32_e32 v42, v42
	v_med3_f32 v50, v61, s82, v139
	v_add_f32_e32 v50, 0x43800000, v50
	v_add_f32_e32 v42, 1.0, v42
	v_rcp_f32_e32 v42, v42
	s_nop 0
	v_mul_f32_e32 v42, v51, v42
	v_mul_f32_e32 v50, v42, v50
	v_mov_b32_e32 v42, v131
	v_cvt_pk_fp8_f32 v42, v43, v45
	v_mov_b32_e32 v43, v131
	v_cvt_pk_fp8_f32 v43, v44, v46
	v_lshlrev_b64 v[44:45], 11, v[136:137]
	v_cvt_pk_fp8_f32 v42, v47, v49 op_sel:[0,0,1]
	v_lshl_add_u64 v[44:45], s[16:17], 0, v[44:45]
	v_cvt_pk_fp8_f32 v43, v48, v50 op_sel:[0,0,1]
	v_lshl_add_u64 v[134:135], v[44:45], 0, v[134:135]
	global_store_dwordx2 v[134:135], v[42:43], off sc1
	s_nop 1
	v_max_f32_e32 v42, v86, v86
	v_min_f32_e32 v42, 0x44e00000, v42
	v_mul_f32_e32 v44, 0x37800000, v42
	v_mul_f32_e32 v42, 0xbc1d265f, v42
	v_exp_f32_e32 v42, v42
	v_med3_f32 v43, v54, s82, v139
	v_add_f32_e32 v43, 0x43800000, v43
	v_add_f32_e32 v42, 1.0, v42
	v_rcp_f32_e32 v42, v42
	s_nop 0
	v_mul_f32_e32 v42, v44, v42
	v_mul_f32_e32 v43, v42, v43
	v_max_f32_e32 v42, v82, v82
	v_min_f32_e32 v42, 0x44e00000, v42
	v_mul_f32_e32 v45, 0x37800000, v42
	v_mul_f32_e32 v42, 0xbc1d265f, v42
	v_exp_f32_e32 v42, v42
	v_med3_f32 v44, v176, s82, v139
	v_add_f32_e32 v44, 0x43800000, v44
	v_add_f32_e32 v42, 1.0, v42
	v_rcp_f32_e32 v42, v42
	s_nop 0
	v_mul_f32_e32 v42, v45, v42
	v_mul_f32_e32 v44, v42, v44
	v_max_f32_e32 v42, v87, v87
	v_min_f32_e32 v42, 0x44e00000, v42
	v_mul_f32_e32 v46, 0x37800000, v42
	v_mul_f32_e32 v42, 0xbc1d265f, v42
	v_exp_f32_e32 v42, v42
	v_med3_f32 v45, v55, s82, v139
	v_add_f32_e32 v45, 0x43800000, v45
	v_add_f32_e32 v42, 1.0, v42
	v_rcp_f32_e32 v42, v42
	s_nop 0
	v_mul_f32_e32 v42, v46, v42
	v_mul_f32_e32 v45, v42, v45
	v_max_f32_e32 v42, v83, v83
	v_min_f32_e32 v42, 0x44e00000, v42
	v_mul_f32_e32 v47, 0x37800000, v42
	v_mul_f32_e32 v42, 0xbc1d265f, v42
	v_exp_f32_e32 v42, v42
	v_med3_f32 v46, v177, s82, v139
	v_add_f32_e32 v46, 0x43800000, v46
	v_add_f32_e32 v42, 1.0, v42
	v_rcp_f32_e32 v42, v42
	s_nop 0
	v_mul_f32_e32 v42, v47, v42
	v_mul_f32_e32 v46, v42, v46
	v_max_f32_e32 v42, v88, v88
	v_min_f32_e32 v42, 0x44e00000, v42
	v_mul_f32_e32 v48, 0x37800000, v42
	v_mul_f32_e32 v42, 0xbc1d265f, v42
	v_exp_f32_e32 v42, v42
	v_med3_f32 v47, v56, s82, v139
	v_add_f32_e32 v47, 0x43800000, v47
	v_add_f32_e32 v42, 1.0, v42
	v_rcp_f32_e32 v42, v42
	s_nop 0
	v_mul_f32_e32 v42, v48, v42
	v_mul_f32_e32 v47, v42, v47
	v_max_f32_e32 v42, v84, v84
	v_min_f32_e32 v42, 0x44e00000, v42
	v_mul_f32_e32 v49, 0x37800000, v42
	v_mul_f32_e32 v42, 0xbc1d265f, v42
	v_exp_f32_e32 v42, v42
	v_med3_f32 v48, v178, s82, v139
	v_add_f32_e32 v48, 0x43800000, v48
	v_add_f32_e32 v42, 1.0, v42
	v_rcp_f32_e32 v42, v42
	s_nop 0
	v_mul_f32_e32 v42, v49, v42
	v_mul_f32_e32 v48, v42, v48
	v_max_f32_e32 v42, v89, v89
	v_min_f32_e32 v42, 0x44e00000, v42
	v_mul_f32_e32 v50, 0x37800000, v42
	v_mul_f32_e32 v42, 0xbc1d265f, v42
	v_exp_f32_e32 v42, v42
	v_med3_f32 v49, v57, s82, v139
	v_add_f32_e32 v49, 0x43800000, v49
	v_add_f32_e32 v42, 1.0, v42
	v_rcp_f32_e32 v42, v42
	s_nop 0
	v_mul_f32_e32 v42, v50, v42
	v_mul_f32_e32 v49, v42, v49
	v_max_f32_e32 v42, v85, v85
	v_min_f32_e32 v42, 0x44e00000, v42
	v_mul_f32_e32 v51, 0x37800000, v42
	v_mul_f32_e32 v42, 0xbc1d265f, v42
	v_exp_f32_e32 v42, v42
	v_med3_f32 v50, v179, s82, v139
	v_add_f32_e32 v50, 0x43800000, v50
	v_add_f32_e32 v42, 1.0, v42
	v_rcp_f32_e32 v42, v42
	s_nop 0
	v_mul_f32_e32 v42, v51, v42
	v_mul_f32_e32 v50, v42, v50
	v_mov_b32_e32 v42, v131
	v_cvt_pk_fp8_f32 v42, v43, v45
	v_mov_b32_e32 v43, v131
	v_cvt_pk_fp8_f32 v43, v44, v46
	v_lshl_add_u64 v[44:45], v[134:135], 0, s[34:35]
	v_cvt_pk_fp8_f32 v42, v47, v49 op_sel:[0,0,1]
	s_mov_b64 s[34:35], 0x10000
	v_cvt_pk_fp8_f32 v43, v48, v50 op_sel:[0,0,1]
	s_nop 0
	global_store_dwordx2 v[44:45], v[42:43], off sc1
	s_nop 1
	v_max_f32_e32 v42, v78, v78
	v_min_f32_e32 v42, 0x44e00000, v42
	v_mul_f32_e32 v44, 0x37800000, v42
	v_mul_f32_e32 v42, 0xbc1d265f, v42
	v_exp_f32_e32 v42, v42
	v_med3_f32 v43, v172, s82, v139
	v_add_f32_e32 v43, 0x43800000, v43
	v_add_f32_e32 v42, 1.0, v42
	v_rcp_f32_e32 v42, v42
	s_nop 0
	v_mul_f32_e32 v42, v44, v42
	v_mul_f32_e32 v43, v42, v43
	v_max_f32_e32 v42, v74, v74
	v_min_f32_e32 v42, 0x44e00000, v42
	v_mul_f32_e32 v45, 0x37800000, v42
	v_mul_f32_e32 v42, 0xbc1d265f, v42
	v_exp_f32_e32 v42, v42
	v_med3_f32 v44, v18, s82, v139
	v_add_f32_e32 v44, 0x43800000, v44
	v_add_f32_e32 v42, 1.0, v42
	v_rcp_f32_e32 v42, v42
	s_nop 0
	v_mul_f32_e32 v42, v45, v42
	v_mul_f32_e32 v44, v42, v44
	v_max_f32_e32 v42, v79, v79
	v_min_f32_e32 v42, 0x44e00000, v42
	v_mul_f32_e32 v46, 0x37800000, v42
	v_mul_f32_e32 v42, 0xbc1d265f, v42
	v_exp_f32_e32 v42, v42
	v_med3_f32 v45, v173, s82, v139
	v_add_f32_e32 v45, 0x43800000, v45
	v_add_f32_e32 v42, 1.0, v42
	v_rcp_f32_e32 v42, v42
	s_nop 0
	v_mul_f32_e32 v42, v46, v42
	v_mul_f32_e32 v45, v42, v45
	v_max_f32_e32 v42, v75, v75
	v_min_f32_e32 v42, 0x44e00000, v42
	v_mul_f32_e32 v47, 0x37800000, v42
	v_mul_f32_e32 v42, 0xbc1d265f, v42
	v_exp_f32_e32 v42, v42
	v_med3_f32 v46, v19, s82, v139
	v_add_f32_e32 v46, 0x43800000, v46
	v_add_f32_e32 v42, 1.0, v42
	v_rcp_f32_e32 v42, v42
	s_nop 0
	v_mul_f32_e32 v42, v47, v42
	v_mul_f32_e32 v46, v42, v46
	v_max_f32_e32 v42, v80, v80
	v_min_f32_e32 v42, 0x44e00000, v42
	v_mul_f32_e32 v48, 0x37800000, v42
	v_mul_f32_e32 v42, 0xbc1d265f, v42
	v_exp_f32_e32 v42, v42
	v_med3_f32 v47, v174, s82, v139
	v_add_f32_e32 v47, 0x43800000, v47
	v_add_f32_e32 v42, 1.0, v42
	v_rcp_f32_e32 v42, v42
	s_nop 0
	v_mul_f32_e32 v42, v48, v42
	v_mul_f32_e32 v47, v42, v47
	v_max_f32_e32 v42, v76, v76
	v_min_f32_e32 v42, 0x44e00000, v42
	v_mul_f32_e32 v49, 0x37800000, v42
	v_mul_f32_e32 v42, 0xbc1d265f, v42
	v_exp_f32_e32 v42, v42
	v_med3_f32 v48, v20, s82, v139
	v_add_f32_e32 v48, 0x43800000, v48
	v_add_f32_e32 v42, 1.0, v42
	v_rcp_f32_e32 v42, v42
	s_nop 0
	v_mul_f32_e32 v42, v49, v42
	v_mul_f32_e32 v48, v42, v48
	v_max_f32_e32 v42, v81, v81
	v_min_f32_e32 v42, 0x44e00000, v42
	v_mul_f32_e32 v50, 0x37800000, v42
	v_mul_f32_e32 v42, 0xbc1d265f, v42
	v_exp_f32_e32 v42, v42
	v_med3_f32 v49, v175, s82, v139
	v_add_f32_e32 v49, 0x43800000, v49
	v_add_f32_e32 v42, 1.0, v42
	v_rcp_f32_e32 v42, v42
	s_nop 0
	v_mul_f32_e32 v42, v50, v42
	v_mul_f32_e32 v49, v42, v49
	v_max_f32_e32 v42, v77, v77
	v_min_f32_e32 v42, 0x44e00000, v42
	v_mul_f32_e32 v51, 0x37800000, v42
	v_mul_f32_e32 v42, 0xbc1d265f, v42
	v_exp_f32_e32 v42, v42
	v_med3_f32 v50, v21, s82, v139
	v_add_f32_e32 v50, 0x43800000, v50
	v_add_f32_e32 v42, 1.0, v42
	v_rcp_f32_e32 v42, v42
	s_nop 0
	v_mul_f32_e32 v42, v51, v42
	v_mul_f32_e32 v50, v42, v50
	v_mov_b32_e32 v42, v131
	v_cvt_pk_fp8_f32 v42, v43, v45
	v_mov_b32_e32 v43, v131
	v_cvt_pk_fp8_f32 v43, v44, v46
	v_lshl_add_u64 v[44:45], v[134:135], 0, s[34:35]
	v_cvt_pk_fp8_f32 v42, v47, v49 op_sel:[0,0,1]
	s_mov_b64 s[34:35], 0x18000
	v_cvt_pk_fp8_f32 v43, v48, v50 op_sel:[0,0,1]
	s_nop 0
	global_store_dwordx2 v[44:45], v[42:43], off sc1
	s_nop 1
	v_max_f32_e32 v42, v70, v70
	v_min_f32_e32 v42, 0x44e00000, v42
	v_mul_f32_e32 v44, 0x37800000, v42
	v_mul_f32_e32 v42, 0xbc1d265f, v42
	v_exp_f32_e32 v42, v42
	v_med3_f32 v43, v6, s82, v139
	v_add_f32_e32 v43, 0x43800000, v43
	v_add_f32_e32 v42, 1.0, v42
	v_rcp_f32_e32 v42, v42
	s_nop 0
	v_mul_f32_e32 v42, v44, v42
	v_mul_f32_e32 v43, v42, v43
	v_max_f32_e32 v42, v66, v66
	v_min_f32_e32 v42, 0x44e00000, v42
	v_mul_f32_e32 v45, 0x37800000, v42
	v_mul_f32_e32 v42, 0xbc1d265f, v42
	v_exp_f32_e32 v42, v42
	v_med3_f32 v44, v14, s82, v139
	v_add_f32_e32 v44, 0x43800000, v44
	v_add_f32_e32 v42, 1.0, v42
	v_rcp_f32_e32 v42, v42
	s_nop 0
	v_mul_f32_e32 v42, v45, v42
	v_mul_f32_e32 v44, v42, v44
	v_max_f32_e32 v42, v71, v71
	v_min_f32_e32 v42, 0x44e00000, v42
	v_mul_f32_e32 v46, 0x37800000, v42
	v_mul_f32_e32 v42, 0xbc1d265f, v42
	v_exp_f32_e32 v42, v42
	v_med3_f32 v45, v7, s82, v139
	v_add_f32_e32 v45, 0x43800000, v45
	v_add_f32_e32 v42, 1.0, v42
	v_rcp_f32_e32 v42, v42
	s_nop 0
	v_mul_f32_e32 v42, v46, v42
	v_mul_f32_e32 v45, v42, v45
	v_max_f32_e32 v42, v67, v67
	v_min_f32_e32 v42, 0x44e00000, v42
	v_mul_f32_e32 v47, 0x37800000, v42
	v_mul_f32_e32 v42, 0xbc1d265f, v42
	v_exp_f32_e32 v42, v42
	v_med3_f32 v46, v15, s82, v139
	v_add_f32_e32 v46, 0x43800000, v46
	v_add_f32_e32 v42, 1.0, v42
	v_rcp_f32_e32 v42, v42
	s_nop 0
	v_mul_f32_e32 v42, v47, v42
	v_mul_f32_e32 v46, v42, v46
	v_max_f32_e32 v42, v72, v72
	v_min_f32_e32 v42, 0x44e00000, v42
	v_mul_f32_e32 v48, 0x37800000, v42
	v_mul_f32_e32 v42, 0xbc1d265f, v42
	v_exp_f32_e32 v42, v42
	v_med3_f32 v47, v8, s82, v139
	v_add_f32_e32 v47, 0x43800000, v47
	v_add_f32_e32 v42, 1.0, v42
	v_rcp_f32_e32 v42, v42
	s_nop 0
	v_mul_f32_e32 v42, v48, v42
	v_mul_f32_e32 v47, v42, v47
	v_max_f32_e32 v42, v68, v68
	v_min_f32_e32 v42, 0x44e00000, v42
	v_mul_f32_e32 v49, 0x37800000, v42
	v_mul_f32_e32 v42, 0xbc1d265f, v42
	v_exp_f32_e32 v42, v42
	v_med3_f32 v48, v16, s82, v139
	v_add_f32_e32 v48, 0x43800000, v48
	v_add_f32_e32 v42, 1.0, v42
	v_rcp_f32_e32 v42, v42
	s_nop 0
	v_mul_f32_e32 v42, v49, v42
	v_mul_f32_e32 v48, v42, v48
	v_max_f32_e32 v42, v73, v73
	v_min_f32_e32 v42, 0x44e00000, v42
	v_mul_f32_e32 v50, 0x37800000, v42
	v_mul_f32_e32 v42, 0xbc1d265f, v42
	v_exp_f32_e32 v42, v42
	v_med3_f32 v49, v9, s82, v139
	v_add_f32_e32 v49, 0x43800000, v49
	v_add_f32_e32 v42, 1.0, v42
	v_rcp_f32_e32 v42, v42
	s_nop 0
	v_mul_f32_e32 v42, v50, v42
	v_mul_f32_e32 v49, v42, v49
	v_max_f32_e32 v42, v69, v69
	v_min_f32_e32 v42, 0x44e00000, v42
	v_mul_f32_e32 v51, 0x37800000, v42
	v_mul_f32_e32 v42, 0xbc1d265f, v42
	v_exp_f32_e32 v42, v42
	v_med3_f32 v50, v17, s82, v139
	v_add_f32_e32 v50, 0x43800000, v50
	v_add_f32_e32 v42, 1.0, v42
	v_rcp_f32_e32 v42, v42
	s_nop 0
	v_mul_f32_e32 v42, v51, v42
	v_mul_f32_e32 v50, v42, v50
	v_mov_b32_e32 v42, v131
	v_cvt_pk_fp8_f32 v42, v43, v45
	v_mov_b32_e32 v43, v131
	v_cvt_pk_fp8_f32 v43, v44, v46
	v_lshl_add_u64 v[44:45], v[134:135], 0, s[34:35]
	v_cvt_pk_fp8_f32 v42, v47, v49 op_sel:[0,0,1]
	s_mov_b64 s[34:35], 0x48000
	v_cvt_pk_fp8_f32 v43, v48, v50 op_sel:[0,0,1]
	s_nop 0
	global_store_dwordx2 v[44:45], v[42:43], off sc1
	s_nop 1
	v_max_f32_e32 v42, v38, v38
	v_min_f32_e32 v42, 0x44e00000, v42
	v_mul_f32_e32 v44, 0x37800000, v42
	v_mul_f32_e32 v42, 0xbc1d265f, v42
	v_exp_f32_e32 v42, v42
	v_med3_f32 v43, v98, s82, v139
	v_add_f32_e32 v43, 0x43800000, v43
	v_add_f32_e32 v42, 1.0, v42
	v_rcp_f32_e32 v42, v42
	s_nop 0
	v_mul_f32_e32 v42, v44, v42
	v_mul_f32_e32 v43, v42, v43
	v_max_f32_e32 v42, v34, v34
	v_min_f32_e32 v42, 0x44e00000, v42
	v_mul_f32_e32 v45, 0x37800000, v42
	v_mul_f32_e32 v42, 0xbc1d265f, v42
	v_exp_f32_e32 v42, v42
	v_med3_f32 v44, v102, s82, v139
	v_add_f32_e32 v44, 0x43800000, v44
	v_add_f32_e32 v42, 1.0, v42
	v_rcp_f32_e32 v42, v42
	s_nop 0
	v_mul_f32_e32 v42, v45, v42
	v_mul_f32_e32 v44, v42, v44
	v_max_f32_e32 v42, v39, v39
	v_min_f32_e32 v42, 0x44e00000, v42
	v_mul_f32_e32 v46, 0x37800000, v42
	v_mul_f32_e32 v42, 0xbc1d265f, v42
	v_exp_f32_e32 v42, v42
	v_med3_f32 v45, v99, s82, v139
	v_add_f32_e32 v45, 0x43800000, v45
	v_add_f32_e32 v42, 1.0, v42
	v_rcp_f32_e32 v42, v42
	s_nop 0
	v_mul_f32_e32 v42, v46, v42
	v_mul_f32_e32 v45, v42, v45
	v_max_f32_e32 v42, v35, v35
	v_min_f32_e32 v42, 0x44e00000, v42
	v_mul_f32_e32 v47, 0x37800000, v42
	v_mul_f32_e32 v42, 0xbc1d265f, v42
	v_exp_f32_e32 v42, v42
	v_med3_f32 v46, v103, s82, v139
	v_add_f32_e32 v46, 0x43800000, v46
	v_add_f32_e32 v42, 1.0, v42
	v_rcp_f32_e32 v42, v42
	s_nop 0
	v_mul_f32_e32 v42, v47, v42
	v_mul_f32_e32 v46, v42, v46
	v_max_f32_e32 v42, v40, v40
	v_min_f32_e32 v42, 0x44e00000, v42
	v_mul_f32_e32 v48, 0x37800000, v42
	v_mul_f32_e32 v42, 0xbc1d265f, v42
	v_exp_f32_e32 v42, v42
	v_med3_f32 v47, v100, s82, v139
	v_add_f32_e32 v47, 0x43800000, v47
	v_add_f32_e32 v42, 1.0, v42
	v_rcp_f32_e32 v42, v42
	s_nop 0
	v_mul_f32_e32 v42, v48, v42
	v_mul_f32_e32 v47, v42, v47
	v_max_f32_e32 v42, v36, v36
	v_min_f32_e32 v42, 0x44e00000, v42
	v_mul_f32_e32 v49, 0x37800000, v42
	v_mul_f32_e32 v42, 0xbc1d265f, v42
	v_exp_f32_e32 v42, v42
	v_med3_f32 v48, v104, s82, v139
	v_add_f32_e32 v48, 0x43800000, v48
	v_add_f32_e32 v42, 1.0, v42
	v_rcp_f32_e32 v42, v42
	s_nop 0
	v_mul_f32_e32 v42, v49, v42
	v_mul_f32_e32 v48, v42, v48
	v_max_f32_e32 v42, v41, v41
	v_min_f32_e32 v42, 0x44e00000, v42
	v_mul_f32_e32 v50, 0x37800000, v42
	v_mul_f32_e32 v42, 0xbc1d265f, v42
	v_exp_f32_e32 v42, v42
	v_med3_f32 v49, v101, s82, v139
	v_add_f32_e32 v49, 0x43800000, v49
	v_add_f32_e32 v42, 1.0, v42
	v_rcp_f32_e32 v42, v42
	s_nop 0
	v_mul_f32_e32 v42, v50, v42
	v_mul_f32_e32 v49, v42, v49
	v_max_f32_e32 v42, v37, v37
	v_min_f32_e32 v42, 0x44e00000, v42
	v_mul_f32_e32 v51, 0x37800000, v42
	v_mul_f32_e32 v42, 0xbc1d265f, v42
	v_exp_f32_e32 v42, v42
	v_med3_f32 v50, v105, s82, v139
	v_add_f32_e32 v50, 0x43800000, v50
	v_add_f32_e32 v42, 1.0, v42
	v_rcp_f32_e32 v42, v42
	s_nop 0
	v_mul_f32_e32 v42, v51, v42
	v_mul_f32_e32 v50, v42, v50
	v_mov_b32_e32 v42, v131
	v_cvt_pk_fp8_f32 v42, v43, v45
	v_mov_b32_e32 v43, v131
	v_cvt_pk_fp8_f32 v43, v44, v46
	v_lshl_add_u64 v[44:45], v[134:135], 0, s[22:23]
	v_cvt_pk_fp8_f32 v42, v47, v49 op_sel:[0,0,1]
	v_cvt_pk_fp8_f32 v43, v48, v50 op_sel:[0,0,1]
	s_nop 0
	global_store_dwordx2 v[44:45], v[42:43], off sc1
	s_nop 1
	v_max_f32_e32 v42, v30, v30
	v_min_f32_e32 v42, 0x44e00000, v42
	v_mul_f32_e32 v44, 0x37800000, v42
	v_mul_f32_e32 v42, 0xbc1d265f, v42
	v_exp_f32_e32 v42, v42
	v_med3_f32 v43, v106, s82, v139
	v_add_f32_e32 v43, 0x43800000, v43
	v_add_f32_e32 v42, 1.0, v42
	v_rcp_f32_e32 v42, v42
	s_nop 0
	v_mul_f32_e32 v42, v44, v42
	v_mul_f32_e32 v43, v42, v43
	v_max_f32_e32 v42, v26, v26
	v_min_f32_e32 v42, 0x44e00000, v42
	v_mul_f32_e32 v45, 0x37800000, v42
	v_mul_f32_e32 v42, 0xbc1d265f, v42
	v_exp_f32_e32 v42, v42
	v_med3_f32 v44, v110, s82, v139
	v_add_f32_e32 v44, 0x43800000, v44
	v_add_f32_e32 v42, 1.0, v42
	v_rcp_f32_e32 v42, v42
	s_nop 0
	v_mul_f32_e32 v42, v45, v42
	v_mul_f32_e32 v44, v42, v44
	v_max_f32_e32 v42, v31, v31
	v_min_f32_e32 v42, 0x44e00000, v42
	v_mul_f32_e32 v46, 0x37800000, v42
	v_mul_f32_e32 v42, 0xbc1d265f, v42
	v_exp_f32_e32 v42, v42
	v_med3_f32 v45, v107, s82, v139
	v_add_f32_e32 v45, 0x43800000, v45
	v_add_f32_e32 v42, 1.0, v42
	v_rcp_f32_e32 v42, v42
	s_nop 0
	v_mul_f32_e32 v42, v46, v42
	v_mul_f32_e32 v45, v42, v45
	v_max_f32_e32 v42, v27, v27
	v_min_f32_e32 v42, 0x44e00000, v42
	v_mul_f32_e32 v47, 0x37800000, v42
	v_mul_f32_e32 v42, 0xbc1d265f, v42
	v_exp_f32_e32 v42, v42
	v_med3_f32 v46, v111, s82, v139
	v_add_f32_e32 v46, 0x43800000, v46
	v_add_f32_e32 v42, 1.0, v42
	v_rcp_f32_e32 v42, v42
	s_nop 0
	v_mul_f32_e32 v42, v47, v42
	v_mul_f32_e32 v46, v42, v46
	v_max_f32_e32 v42, v32, v32
	v_min_f32_e32 v42, 0x44e00000, v42
	v_mul_f32_e32 v48, 0x37800000, v42
	v_mul_f32_e32 v42, 0xbc1d265f, v42
	v_exp_f32_e32 v42, v42
	v_med3_f32 v47, v108, s82, v139
	v_add_f32_e32 v47, 0x43800000, v47
	v_add_f32_e32 v42, 1.0, v42
	v_rcp_f32_e32 v42, v42
	s_nop 0
	v_mul_f32_e32 v42, v48, v42
	v_mul_f32_e32 v47, v42, v47
	v_max_f32_e32 v42, v28, v28
	v_min_f32_e32 v42, 0x44e00000, v42
	v_mul_f32_e32 v49, 0x37800000, v42
	v_mul_f32_e32 v42, 0xbc1d265f, v42
	v_exp_f32_e32 v42, v42
	v_med3_f32 v48, v112, s82, v139
	v_add_f32_e32 v48, 0x43800000, v48
	v_add_f32_e32 v42, 1.0, v42
	v_rcp_f32_e32 v42, v42
	s_nop 0
	v_mul_f32_e32 v42, v49, v42
	v_mul_f32_e32 v48, v42, v48
	v_max_f32_e32 v42, v33, v33
	v_min_f32_e32 v42, 0x44e00000, v42
	v_mul_f32_e32 v50, 0x37800000, v42
	v_mul_f32_e32 v42, 0xbc1d265f, v42
	v_exp_f32_e32 v42, v42
	v_med3_f32 v49, v109, s82, v139
	v_add_f32_e32 v49, 0x43800000, v49
	v_add_f32_e32 v42, 1.0, v42
	v_rcp_f32_e32 v42, v42
	s_nop 0
	v_mul_f32_e32 v42, v50, v42
	v_mul_f32_e32 v49, v42, v49
	v_max_f32_e32 v42, v29, v29
	v_min_f32_e32 v42, 0x44e00000, v42
	v_mul_f32_e32 v51, 0x37800000, v42
	v_mul_f32_e32 v42, 0xbc1d265f, v42
	v_exp_f32_e32 v42, v42
	v_med3_f32 v50, v113, s82, v139
	v_add_f32_e32 v50, 0x43800000, v50
	v_add_f32_e32 v42, 1.0, v42
	v_rcp_f32_e32 v42, v42
	s_nop 0
	v_mul_f32_e32 v42, v51, v42
	v_mul_f32_e32 v50, v42, v50
	v_mov_b32_e32 v42, v131
	v_cvt_pk_fp8_f32 v42, v43, v45
	v_mov_b32_e32 v43, v131
	v_cvt_pk_fp8_f32 v43, v44, v46
	v_lshl_add_u64 v[44:45], v[134:135], 0, s[34:35]
	v_cvt_pk_fp8_f32 v42, v47, v49 op_sel:[0,0,1]
	s_mov_b64 s[34:35], 0x50000
	v_cvt_pk_fp8_f32 v43, v48, v50 op_sel:[0,0,1]
	s_nop 0
	global_store_dwordx2 v[44:45], v[42:43], off sc1
	s_nop 1
	v_max_f32_e32 v42, v22, v22
	v_min_f32_e32 v42, 0x44e00000, v42
	v_mul_f32_e32 v44, 0x37800000, v42
	v_mul_f32_e32 v42, 0xbc1d265f, v42
	v_exp_f32_e32 v42, v42
	v_med3_f32 v43, v114, s82, v139
	v_add_f32_e32 v43, 0x43800000, v43
	v_add_f32_e32 v42, 1.0, v42
	v_rcp_f32_e32 v42, v42
	s_nop 0
	v_mul_f32_e32 v42, v44, v42
	v_mul_f32_e32 v43, v42, v43
	v_max_f32_e32 v42, v220, v220
	v_min_f32_e32 v42, 0x44e00000, v42
	v_mul_f32_e32 v45, 0x37800000, v42
	v_mul_f32_e32 v42, 0xbc1d265f, v42
	v_exp_f32_e32 v42, v42
	v_med3_f32 v44, v118, s82, v139
	v_add_f32_e32 v44, 0x43800000, v44
	v_add_f32_e32 v42, 1.0, v42
	v_rcp_f32_e32 v42, v42
	s_nop 0
	v_mul_f32_e32 v42, v45, v42
	v_mul_f32_e32 v44, v42, v44
	v_max_f32_e32 v42, v23, v23
	v_min_f32_e32 v42, 0x44e00000, v42
	v_mul_f32_e32 v46, 0x37800000, v42
	v_mul_f32_e32 v42, 0xbc1d265f, v42
	v_exp_f32_e32 v42, v42
	v_med3_f32 v45, v115, s82, v139
	v_add_f32_e32 v45, 0x43800000, v45
	v_add_f32_e32 v42, 1.0, v42
	v_rcp_f32_e32 v42, v42
	s_nop 0
	v_mul_f32_e32 v42, v46, v42
	v_mul_f32_e32 v45, v42, v45
	v_max_f32_e32 v42, v221, v221
	v_min_f32_e32 v42, 0x44e00000, v42
	v_mul_f32_e32 v47, 0x37800000, v42
	v_mul_f32_e32 v42, 0xbc1d265f, v42
	v_exp_f32_e32 v42, v42
	v_med3_f32 v46, v119, s82, v139
	v_add_f32_e32 v46, 0x43800000, v46
	v_add_f32_e32 v42, 1.0, v42
	v_rcp_f32_e32 v42, v42
	s_nop 0
	v_mul_f32_e32 v42, v47, v42
	v_mul_f32_e32 v46, v42, v46
	v_max_f32_e32 v42, v24, v24
	v_min_f32_e32 v42, 0x44e00000, v42
	v_mul_f32_e32 v48, 0x37800000, v42
	v_mul_f32_e32 v42, 0xbc1d265f, v42
	v_exp_f32_e32 v42, v42
	v_med3_f32 v47, v116, s82, v139
	v_add_f32_e32 v47, 0x43800000, v47
	v_add_f32_e32 v42, 1.0, v42
	v_rcp_f32_e32 v42, v42
	s_nop 0
	v_mul_f32_e32 v42, v48, v42
	v_mul_f32_e32 v47, v42, v47
	v_max_f32_e32 v42, v222, v222
	v_min_f32_e32 v42, 0x44e00000, v42
	v_mul_f32_e32 v49, 0x37800000, v42
	v_mul_f32_e32 v42, 0xbc1d265f, v42
	v_exp_f32_e32 v42, v42
	v_med3_f32 v48, v120, s82, v139
	v_add_f32_e32 v48, 0x43800000, v48
	v_add_f32_e32 v42, 1.0, v42
	v_rcp_f32_e32 v42, v42
	s_nop 0
	v_mul_f32_e32 v42, v49, v42
	v_mul_f32_e32 v48, v42, v48
	v_max_f32_e32 v42, v25, v25
	v_min_f32_e32 v42, 0x44e00000, v42
	v_mul_f32_e32 v50, 0x37800000, v42
	v_mul_f32_e32 v42, 0xbc1d265f, v42
	v_exp_f32_e32 v42, v42
	v_med3_f32 v49, v117, s82, v139
	v_add_f32_e32 v49, 0x43800000, v49
	v_add_f32_e32 v42, 1.0, v42
	v_rcp_f32_e32 v42, v42
	s_nop 0
	v_mul_f32_e32 v42, v50, v42
	v_mul_f32_e32 v49, v42, v49
	v_max_f32_e32 v42, v223, v223
	v_min_f32_e32 v42, 0x44e00000, v42
	v_mul_f32_e32 v51, 0x37800000, v42
	v_mul_f32_e32 v42, 0xbc1d265f, v42
	v_exp_f32_e32 v42, v42
	v_med3_f32 v50, v121, s82, v139
	v_add_f32_e32 v50, 0x43800000, v50
	v_add_f32_e32 v42, 1.0, v42
	v_rcp_f32_e32 v42, v42
	s_nop 0
	v_mul_f32_e32 v42, v51, v42
	v_mul_f32_e32 v50, v42, v50
	v_mov_b32_e32 v42, v131
	v_cvt_pk_fp8_f32 v42, v43, v45
	v_mov_b32_e32 v43, v131
	v_cvt_pk_fp8_f32 v43, v44, v46
	v_lshl_add_u64 v[44:45], v[134:135], 0, s[34:35]
	v_cvt_pk_fp8_f32 v42, v47, v49 op_sel:[0,0,1]
	s_mov_b64 s[34:35], 0x58000
	v_cvt_pk_fp8_f32 v43, v48, v50 op_sel:[0,0,1]
	s_nop 0
	global_store_dwordx2 v[44:45], v[42:43], off sc1
	s_nop 1
	v_max_f32_e32 v42, v2, v2
	v_min_f32_e32 v42, 0x44e00000, v42
	v_mul_f32_e32 v44, 0x37800000, v42
	v_mul_f32_e32 v42, 0xbc1d265f, v42
	v_exp_f32_e32 v42, v42
	v_med3_f32 v43, v122, s82, v139
	v_add_f32_e32 v43, 0x43800000, v43
	v_add_f32_e32 v42, 1.0, v42
	v_rcp_f32_e32 v42, v42
	s_nop 0
	v_mul_f32_e32 v42, v44, v42
	v_mul_f32_e32 v43, v42, v43
	v_max_f32_e32 v42, v10, v10
	v_min_f32_e32 v42, 0x44e00000, v42
	v_mul_f32_e32 v45, 0x37800000, v42
	v_mul_f32_e32 v42, 0xbc1d265f, v42
	v_exp_f32_e32 v42, v42
	v_med3_f32 v44, v126, s82, v139
	v_add_f32_e32 v44, 0x43800000, v44
	v_add_f32_e32 v42, 1.0, v42
	v_rcp_f32_e32 v42, v42
	s_nop 0
	v_mul_f32_e32 v42, v45, v42
	v_mul_f32_e32 v44, v42, v44
	v_max_f32_e32 v42, v3, v3
	v_min_f32_e32 v42, 0x44e00000, v42
	v_mul_f32_e32 v46, 0x37800000, v42
	v_mul_f32_e32 v42, 0xbc1d265f, v42
	v_exp_f32_e32 v42, v42
	v_med3_f32 v45, v123, s82, v139
	v_add_f32_e32 v45, 0x43800000, v45
	v_add_f32_e32 v42, 1.0, v42
	v_rcp_f32_e32 v42, v42
	s_nop 0
	v_mul_f32_e32 v42, v46, v42
	v_mul_f32_e32 v45, v42, v45
	v_max_f32_e32 v42, v11, v11
	v_min_f32_e32 v42, 0x44e00000, v42
	v_mul_f32_e32 v47, 0x37800000, v42
	v_mul_f32_e32 v42, 0xbc1d265f, v42
	v_exp_f32_e32 v42, v42
	v_med3_f32 v46, v127, s82, v139
	v_add_f32_e32 v46, 0x43800000, v46
	v_add_f32_e32 v42, 1.0, v42
	v_rcp_f32_e32 v42, v42
	s_nop 0
	v_mul_f32_e32 v42, v47, v42
	v_mul_f32_e32 v46, v42, v46
	v_max_f32_e32 v42, v4, v4
	v_min_f32_e32 v42, 0x44e00000, v42
	v_mul_f32_e32 v48, 0x37800000, v42
	v_mul_f32_e32 v42, 0xbc1d265f, v42
	v_exp_f32_e32 v42, v42
	v_med3_f32 v47, v124, s82, v139
	v_add_f32_e32 v47, 0x43800000, v47
	v_add_f32_e32 v42, 1.0, v42
	v_rcp_f32_e32 v42, v42
	s_nop 0
	v_mul_f32_e32 v42, v48, v42
	v_mul_f32_e32 v47, v42, v47
	v_max_f32_e32 v42, v12, v12
	v_min_f32_e32 v42, 0x44e00000, v42
	v_mul_f32_e32 v49, 0x37800000, v42
	v_mul_f32_e32 v42, 0xbc1d265f, v42
	v_exp_f32_e32 v42, v42
	v_med3_f32 v48, v128, s82, v139
	v_add_f32_e32 v48, 0x43800000, v48
	v_add_f32_e32 v42, 1.0, v42
	v_rcp_f32_e32 v42, v42
	s_nop 0
	v_mul_f32_e32 v42, v49, v42
	v_mul_f32_e32 v48, v42, v48
	v_max_f32_e32 v42, v5, v5
	v_min_f32_e32 v42, 0x44e00000, v42
	v_mul_f32_e32 v50, 0x37800000, v42
	v_mul_f32_e32 v42, 0xbc1d265f, v42
	v_exp_f32_e32 v42, v42
	v_med3_f32 v49, v125, s82, v139
	v_add_f32_e32 v49, 0x43800000, v49
	v_add_f32_e32 v42, 1.0, v42
	v_rcp_f32_e32 v42, v42
	s_nop 0
	v_mul_f32_e32 v42, v50, v42
	v_mul_f32_e32 v49, v42, v49
	v_max_f32_e32 v42, v13, v13
	v_min_f32_e32 v42, 0x44e00000, v42
	v_mul_f32_e32 v51, 0x37800000, v42
	v_mul_f32_e32 v42, 0xbc1d265f, v42
	v_exp_f32_e32 v42, v42
	v_med3_f32 v50, v129, s82, v139
	v_add_f32_e32 v50, 0x43800000, v50
	v_add_f32_e32 v42, 1.0, v42
	v_rcp_f32_e32 v42, v42
	s_nop 0
	v_mul_f32_e32 v42, v51, v42
	v_mul_f32_e32 v50, v42, v50
	v_mov_b32_e32 v42, v131
	v_cvt_pk_fp8_f32 v42, v43, v45
	v_mov_b32_e32 v43, v131
	v_cvt_pk_fp8_f32 v43, v44, v46
	v_lshl_add_u64 v[44:45], v[134:135], 0, s[34:35]
	v_cvt_pk_fp8_f32 v42, v47, v49 op_sel:[0,0,1]
	v_cvt_pk_fp8_f32 v43, v48, v50 op_sel:[0,0,1]
	s_nop 0
	global_store_dwordx2 v[44:45], v[42:43], off sc1
	s_nop 1
	s_cbranch_vccnz .LBB0_1236
	s_ashr_i32 s49, s48, 31
	v_readlane_b32 s88, v254, 4
	s_lshl_b64 s[8:9], s[48:49], 14
	v_readlane_b32 s92, v254, 8
	v_readlane_b32 s93, v254, 9
	s_add_u32 s2, s92, s8
	v_mov_b32_e32 v2, v131
	s_addc_u32 s26, s93, s9
	s_lshl_b32 s8, s50, 7
	s_ashr_i32 s9, s8, 31
	v_mbcnt_lo_u32_b32 v2, -1, v2
	s_lshl_b64 s[8:9], s[8:9], 2
	v_mbcnt_hi_u32_b32 v2, -1, v2
	s_add_u32 s2, s2, s8
	s_addc_u32 s9, s26, s9
	s_lshl_b32 s8, s5, 2
	v_ashrrev_i32_e32 v2, 1, v2
	s_add_u32 s8, s2, s8
	v_and_b32_e32 v2, -8, v2
	s_addc_u32 s9, s9, 0
	v_ashrrev_i32_e32 v3, 31, v2
	v_lshl_add_u64 v[6:7], v[2:3], 2, s[8:9]
	v_lshl_add_u64 v[14:15], v[6:7], 0, s[18:19]
	v_add_co_u32_e32 v6, vcc, 0x2000, v6
	v_readlane_b32 s89, v254, 5
	s_nop 0
	v_addc_co_u32_e32 v7, vcc, 0, v7, vcc
	s_nop 0
	s_andn2_b64 vcc, exec, s[28:29]
	v_readlane_b32 s90, v254, 6
	v_readlane_b32 s91, v254, 7
	v_readlane_b32 s94, v254, 10
	v_readlane_b32 s95, v254, 11
	s_cbranch_vccnz .LBB0_1235
	s_barrier
.LBB0_1235:
	s_waitcnt vmcnt(8)
	v_pk_mul_f32 v[4:5], v[142:143], s[42:43] op_sel_hi:[1,0]
	v_pk_mul_f32 v[8:9], v[146:147], s[42:43] op_sel_hi:[1,0]
	v_pk_mul_f32 v[12:13], v[150:151], s[42:43] op_sel_hi:[1,0]
	v_pk_mul_f32 v[16:17], v[154:155], s[42:43] op_sel_hi:[1,0]
	v_pk_mul_f32 v[2:3], v[140:141], s[42:43] op_sel_hi:[1,0]
	v_pk_mul_f32 v[6:7], v[144:145], s[42:43] op_sel_hi:[1,0]
	v_pk_mul_f32 v[10:11], v[148:149], s[42:43] op_sel_hi:[1,0]
	v_pk_mul_f32 v[14:15], v[152:153], s[42:43] op_sel_hi:[1,0]
	v_mov_b64_e32 v[222:223], v[12:13]
	v_mov_b64_e32 v[24:25], v[4:5]
	v_mov_b64_e32 v[28:29], v[12:13]
	v_mov_b64_e32 v[32:33], v[4:5]
	v_mov_b64_e32 v[36:37], v[12:13]
	v_mov_b64_e32 v[40:41], v[4:5]
	v_mov_b64_e32 v[20:21], v[16:17]
	v_mov_b64_e32 v[174:175], v[8:9]
	v_mov_b64_e32 v[178:179], v[16:17]
	v_mov_b64_e32 v[56:57], v[8:9]
	v_mov_b64_e32 v[60:61], v[16:17]
	v_mov_b64_e32 v[64:65], v[8:9]
	v_mov_b64_e32 v[68:69], v[12:13]
	v_mov_b64_e32 v[72:73], v[4:5]
	v_mov_b64_e32 v[76:77], v[12:13]
	v_mov_b64_e32 v[80:81], v[4:5]
	v_mov_b64_e32 v[84:85], v[12:13]
	v_mov_b64_e32 v[88:89], v[4:5]
	v_mov_b64_e32 v[92:93], v[12:13]
	v_mov_b64_e32 v[96:97], v[4:5]
	v_mov_b64_e32 v[100:101], v[8:9]
	v_mov_b64_e32 v[104:105], v[16:17]
	v_mov_b64_e32 v[108:109], v[8:9]
	v_mov_b64_e32 v[112:113], v[16:17]
	v_mov_b64_e32 v[116:117], v[8:9]
	v_mov_b64_e32 v[120:121], v[16:17]
	v_mov_b64_e32 v[124:125], v[8:9]
	v_mov_b64_e32 v[128:129], v[16:17]
	v_readlane_b32 s8, v255, 5
	v_mov_b64_e32 v[220:221], v[10:11]
	v_mov_b64_e32 v[22:23], v[2:3]
	v_mov_b64_e32 v[26:27], v[10:11]
	v_mov_b64_e32 v[30:31], v[2:3]
	v_mov_b64_e32 v[34:35], v[10:11]
	v_mov_b64_e32 v[38:39], v[2:3]
	v_mov_b64_e32 v[18:19], v[14:15]
	v_mov_b64_e32 v[172:173], v[6:7]
	v_mov_b64_e32 v[176:177], v[14:15]
	v_mov_b64_e32 v[54:55], v[6:7]
	v_mov_b64_e32 v[58:59], v[14:15]
	v_mov_b64_e32 v[62:63], v[6:7]
	v_mov_b64_e32 v[66:67], v[10:11]
	v_mov_b64_e32 v[70:71], v[2:3]
	v_mov_b64_e32 v[74:75], v[10:11]
	v_mov_b64_e32 v[78:79], v[2:3]
	v_mov_b64_e32 v[82:83], v[10:11]
	v_mov_b64_e32 v[86:87], v[2:3]
	v_mov_b64_e32 v[90:91], v[10:11]
	v_mov_b64_e32 v[94:95], v[2:3]
	v_mov_b64_e32 v[98:99], v[6:7]
	v_mov_b64_e32 v[102:103], v[14:15]
	v_mov_b64_e32 v[106:107], v[6:7]
	v_mov_b64_e32 v[110:111], v[14:15]
	v_mov_b64_e32 v[114:115], v[6:7]
	v_mov_b64_e32 v[118:119], v[14:15]
	v_mov_b64_e32 v[122:123], v[6:7]
	v_mov_b64_e32 v[126:127], v[14:15]
	s_mov_b32 s2, s48
	s_mov_b32 s26, s50
	s_mov_b32 s49, s85
	s_mov_b32 s75, s43
	s_mov_b32 s84, s69
	s_mov_b32 s80, s8
	v_readlane_b32 s9, v255, 6
	s_andn2_b64 vcc, exec, s[52:53]
	s_cbranch_vccnz .LBB0_1237
	s_branch .LBB0_1238

.LBB0_1265:
	s_and_b64 vcc, exec, s[4:5]
	s_cbranch_vccnz .Lbh_skip_b
	v_readlane_b32 s100, v254, 8
	v_readlane_b32 s101, v254, 9
	s_lshl_b32 s98, s44, 14
	v_mbcnt_lo_u32_b32 v156, -1, 0
	s_add_u32 s100, s100, s98
	s_addc_u32 s101, s101, 0
	s_lshl_b32 s98, s46, 9
	v_mbcnt_hi_u32_b32 v156, -1, v156
	s_add_u32 s100, s100, s98
	s_addc_u32 s101, s101, 0
	s_lshl_b32 s98, s63, 2
	v_ashrrev_i32_e32 v156, 1, v156
	s_add_u32 s100, s100, s98
	s_addc_u32 s101, s101, 0
	v_and_b32_e32 v156, -8, v156
	v_ashrrev_i32_e32 v157, 31, v156
	v_lshl_add_u64 v[156:157], v[156:157], 2, s[100:101]
	s_movk_i32 s100, 0x2000
	s_mov_b32 s101, 0
	v_lshl_add_u64 v[158:159], v[156:157], 0, s[6:7]
	global_load_dwordx4 v[148:151], v[156:157], off offset:16
	global_load_dwordx4 v[140:143], v[156:157], off
	v_lshl_add_u64 v[156:157], v[156:157], 0, s[100:101]
	global_load_dwordx4 v[152:155], v[158:159], off offset:16
	global_load_dwordx4 v[144:147], v[156:157], off
.Lbh_skip_b:
	s_add_u32 s54, s45, 0xffffff00
	s_addc_u32 s55, s47, -1
	s_lshl_b32 s34, s64, 2
	s_add_i32 s34, s34, 0
	s_add_i32 s34, s34, 0x24080
	v_mov_b32_e32 v42, v131
	v_mov_b32_e32 v43, s34
	ds_read_b32 v43, v43
	v_mbcnt_lo_u32_b32 v42, -1, v42
	s_lshl_b32 s34, s65, 8
	v_mbcnt_hi_u32_b32 v42, -1, v42
	s_add_i32 s34, s34, s77
	v_ashrrev_i32_e32 v44, 1, v42
	v_and_or_b32 v42, v42, 15, s34
	s_lshl_b32 s35, s22, 7
	s_waitcnt lgkmcnt(0)
	v_add_u32_e32 v136, v42, v43
	v_max_f32_e32 v42, v94, v94
	v_and_b32_e32 v44, -8, v44
	s_or_b32 s35, s35, s63
	v_min_f32_e32 v42, 0x44e00000, v42
	v_add_u32_e32 v134, s35, v44
	v_mul_f32_e32 v44, 0x37800000, v42
	v_mul_f32_e32 v42, 0xbc1d265f, v42
	v_exp_f32_e32 v42, v42
	v_med3_f32 v43, v62, s81, v139
	v_add_f32_e32 v43, 0x43800000, v43
	v_ashrrev_i32_e32 v137, 31, v136
	v_add_f32_e32 v42, 1.0, v42
	v_rcp_f32_e32 v42, v42
	v_ashrrev_i32_e32 v135, 31, v134
	s_mov_b64 s[34:35], 0x8000
	s_and_b64 vcc, exec, s[4:5]
	v_mul_f32_e32 v42, v44, v42
	v_mul_f32_e32 v43, v42, v43
	v_max_f32_e32 v42, v90, v90
	v_min_f32_e32 v42, 0x44e00000, v42
	v_mul_f32_e32 v45, 0x37800000, v42
	v_mul_f32_e32 v42, 0xbc1d265f, v42
	v_exp_f32_e32 v42, v42
	v_med3_f32 v44, v58, s81, v139
	v_add_f32_e32 v44, 0x43800000, v44
	v_add_f32_e32 v42, 1.0, v42
	v_rcp_f32_e32 v42, v42
	s_nop 0
	v_mul_f32_e32 v42, v45, v42
	v_mul_f32_e32 v44, v42, v44
	v_max_f32_e32 v42, v95, v95
	v_min_f32_e32 v42, 0x44e00000, v42
	v_mul_f32_e32 v46, 0x37800000, v42
	v_mul_f32_e32 v42, 0xbc1d265f, v42
	v_exp_f32_e32 v42, v42
	v_med3_f32 v45, v63, s81, v139
	v_add_f32_e32 v45, 0x43800000, v45
	v_add_f32_e32 v42, 1.0, v42
	v_rcp_f32_e32 v42, v42
	s_nop 0
	v_mul_f32_e32 v42, v46, v42
	v_mul_f32_e32 v45, v42, v45
	v_max_f32_e32 v42, v91, v91
	v_min_f32_e32 v42, 0x44e00000, v42
	v_mul_f32_e32 v47, 0x37800000, v42
	v_mul_f32_e32 v42, 0xbc1d265f, v42
	v_exp_f32_e32 v42, v42
	v_med3_f32 v46, v59, s81, v139
	v_add_f32_e32 v46, 0x43800000, v46
	v_add_f32_e32 v42, 1.0, v42
	v_rcp_f32_e32 v42, v42
	s_nop 0
	v_mul_f32_e32 v42, v47, v42
	v_mul_f32_e32 v46, v42, v46
	v_max_f32_e32 v42, v96, v96
	v_min_f32_e32 v42, 0x44e00000, v42
	v_mul_f32_e32 v48, 0x37800000, v42
	v_mul_f32_e32 v42, 0xbc1d265f, v42
	v_exp_f32_e32 v42, v42
	v_med3_f32 v47, v64, s81, v139
	v_add_f32_e32 v47, 0x43800000, v47
	v_add_f32_e32 v42, 1.0, v42
	v_rcp_f32_e32 v42, v42
	s_nop 0
	v_mul_f32_e32 v42, v48, v42
	v_mul_f32_e32 v47, v42, v47
	v_max_f32_e32 v42, v92, v92
	v_min_f32_e32 v42, 0x44e00000, v42
	v_mul_f32_e32 v49, 0x37800000, v42
	v_mul_f32_e32 v42, 0xbc1d265f, v42
	v_exp_f32_e32 v42, v42
	v_med3_f32 v48, v60, s81, v139
	v_add_f32_e32 v48, 0x43800000, v48
	v_add_f32_e32 v42, 1.0, v42
	v_rcp_f32_e32 v42, v42
	s_nop 0
	v_mul_f32_e32 v42, v49, v42
	v_mul_f32_e32 v48, v42, v48
	v_max_f32_e32 v42, v97, v97
	v_min_f32_e32 v42, 0x44e00000, v42
	v_mul_f32_e32 v50, 0x37800000, v42
	v_mul_f32_e32 v42, 0xbc1d265f, v42
	v_exp_f32_e32 v42, v42
	v_med3_f32 v49, v65, s81, v139
	v_add_f32_e32 v49, 0x43800000, v49
	v_add_f32_e32 v42, 1.0, v42
	v_rcp_f32_e32 v42, v42
	s_nop 0
	v_mul_f32_e32 v42, v50, v42
	v_mul_f32_e32 v49, v42, v49
	v_max_f32_e32 v42, v93, v93
	v_min_f32_e32 v42, 0x44e00000, v42
	v_mul_f32_e32 v51, 0x37800000, v42
	v_mul_f32_e32 v42, 0xbc1d265f, v42
	v_exp_f32_e32 v42, v42
	v_med3_f32 v50, v61, s81, v139
	v_add_f32_e32 v50, 0x43800000, v50
	v_add_f32_e32 v42, 1.0, v42
	v_rcp_f32_e32 v42, v42
	s_nop 0
	v_mul_f32_e32 v42, v51, v42
	v_mul_f32_e32 v50, v42, v50
	v_mov_b32_e32 v42, v131
	v_cvt_pk_fp8_f32 v42, v43, v45
	v_mov_b32_e32 v43, v131
	v_cvt_pk_fp8_f32 v43, v44, v46
	v_lshlrev_b64 v[44:45], 11, v[136:137]
	v_cvt_pk_fp8_f32 v42, v47, v49 op_sel:[0,0,1]
	v_lshl_add_u64 v[44:45], s[16:17], 0, v[44:45]
	v_cvt_pk_fp8_f32 v43, v48, v50 op_sel:[0,0,1]
	v_lshl_add_u64 v[134:135], v[44:45], 0, v[134:135]
	global_store_dwordx2 v[134:135], v[42:43], off sc1
	s_nop 1
	v_max_f32_e32 v42, v86, v86
	v_min_f32_e32 v42, 0x44e00000, v42
	v_mul_f32_e32 v44, 0x37800000, v42
	v_mul_f32_e32 v42, 0xbc1d265f, v42
	v_exp_f32_e32 v42, v42
	v_med3_f32 v43, v54, s81, v139
	v_add_f32_e32 v43, 0x43800000, v43
	v_add_f32_e32 v42, 1.0, v42
	v_rcp_f32_e32 v42, v42
	s_nop 0
	v_mul_f32_e32 v42, v44, v42
	v_mul_f32_e32 v43, v42, v43
	v_max_f32_e32 v42, v82, v82
	v_min_f32_e32 v42, 0x44e00000, v42
	v_mul_f32_e32 v45, 0x37800000, v42
	v_mul_f32_e32 v42, 0xbc1d265f, v42
	v_exp_f32_e32 v42, v42
	v_med3_f32 v44, v176, s81, v139
	v_add_f32_e32 v44, 0x43800000, v44
	v_add_f32_e32 v42, 1.0, v42
	v_rcp_f32_e32 v42, v42
	s_nop 0
	v_mul_f32_e32 v42, v45, v42
	v_mul_f32_e32 v44, v42, v44
	v_max_f32_e32 v42, v87, v87
	v_min_f32_e32 v42, 0x44e00000, v42
	v_mul_f32_e32 v46, 0x37800000, v42
	v_mul_f32_e32 v42, 0xbc1d265f, v42
	v_exp_f32_e32 v42, v42
	v_med3_f32 v45, v55, s81, v139
	v_add_f32_e32 v45, 0x43800000, v45
	v_add_f32_e32 v42, 1.0, v42
	v_rcp_f32_e32 v42, v42
	s_nop 0
	v_mul_f32_e32 v42, v46, v42
	v_mul_f32_e32 v45, v42, v45
	v_max_f32_e32 v42, v83, v83
	v_min_f32_e32 v42, 0x44e00000, v42
	v_mul_f32_e32 v47, 0x37800000, v42
	v_mul_f32_e32 v42, 0xbc1d265f, v42
	v_exp_f32_e32 v42, v42
	v_med3_f32 v46, v177, s81, v139
	v_add_f32_e32 v46, 0x43800000, v46
	v_add_f32_e32 v42, 1.0, v42
	v_rcp_f32_e32 v42, v42
	s_nop 0
	v_mul_f32_e32 v42, v47, v42
	v_mul_f32_e32 v46, v42, v46
	v_max_f32_e32 v42, v88, v88
	v_min_f32_e32 v42, 0x44e00000, v42
	v_mul_f32_e32 v48, 0x37800000, v42
	v_mul_f32_e32 v42, 0xbc1d265f, v42
	v_exp_f32_e32 v42, v42
	v_med3_f32 v47, v56, s81, v139
	v_add_f32_e32 v47, 0x43800000, v47
	v_add_f32_e32 v42, 1.0, v42
	v_rcp_f32_e32 v42, v42
	s_nop 0
	v_mul_f32_e32 v42, v48, v42
	v_mul_f32_e32 v47, v42, v47
	v_max_f32_e32 v42, v84, v84
	v_min_f32_e32 v42, 0x44e00000, v42
	v_mul_f32_e32 v49, 0x37800000, v42
	v_mul_f32_e32 v42, 0xbc1d265f, v42
	v_exp_f32_e32 v42, v42
	v_med3_f32 v48, v178, s81, v139
	v_add_f32_e32 v48, 0x43800000, v48
	v_add_f32_e32 v42, 1.0, v42
	v_rcp_f32_e32 v42, v42
	s_nop 0
	v_mul_f32_e32 v42, v49, v42
	v_mul_f32_e32 v48, v42, v48
	v_max_f32_e32 v42, v89, v89
	v_min_f32_e32 v42, 0x44e00000, v42
	v_mul_f32_e32 v50, 0x37800000, v42
	v_mul_f32_e32 v42, 0xbc1d265f, v42
	v_exp_f32_e32 v42, v42
	v_med3_f32 v49, v57, s81, v139
	v_add_f32_e32 v49, 0x43800000, v49
	v_add_f32_e32 v42, 1.0, v42
	v_rcp_f32_e32 v42, v42
	s_nop 0
	v_mul_f32_e32 v42, v50, v42
	v_mul_f32_e32 v49, v42, v49
	v_max_f32_e32 v42, v85, v85
	v_min_f32_e32 v42, 0x44e00000, v42
	v_mul_f32_e32 v51, 0x37800000, v42
	v_mul_f32_e32 v42, 0xbc1d265f, v42
	v_exp_f32_e32 v42, v42
	v_med3_f32 v50, v179, s81, v139
	v_add_f32_e32 v50, 0x43800000, v50
	v_add_f32_e32 v42, 1.0, v42
	v_rcp_f32_e32 v42, v42
	s_nop 0
	v_mul_f32_e32 v42, v51, v42
	v_mul_f32_e32 v50, v42, v50
	v_mov_b32_e32 v42, v131
	v_cvt_pk_fp8_f32 v42, v43, v45
	v_mov_b32_e32 v43, v131
	v_cvt_pk_fp8_f32 v43, v44, v46
	v_lshl_add_u64 v[44:45], v[134:135], 0, s[34:35]
	v_cvt_pk_fp8_f32 v42, v47, v49 op_sel:[0,0,1]
	s_mov_b64 s[34:35], 0x10000
	v_cvt_pk_fp8_f32 v43, v48, v50 op_sel:[0,0,1]
	s_nop 0
	global_store_dwordx2 v[44:45], v[42:43], off sc1
	s_nop 1
	v_max_f32_e32 v42, v78, v78
	v_min_f32_e32 v42, 0x44e00000, v42
	v_mul_f32_e32 v44, 0x37800000, v42
	v_mul_f32_e32 v42, 0xbc1d265f, v42
	v_exp_f32_e32 v42, v42
	v_med3_f32 v43, v172, s81, v139
	v_add_f32_e32 v43, 0x43800000, v43
	v_add_f32_e32 v42, 1.0, v42
	v_rcp_f32_e32 v42, v42
	s_nop 0
	v_mul_f32_e32 v42, v44, v42
	v_mul_f32_e32 v43, v42, v43
	v_max_f32_e32 v42, v74, v74
	v_min_f32_e32 v42, 0x44e00000, v42
	v_mul_f32_e32 v45, 0x37800000, v42
	v_mul_f32_e32 v42, 0xbc1d265f, v42
	v_exp_f32_e32 v42, v42
	v_med3_f32 v44, v18, s81, v139
	v_add_f32_e32 v44, 0x43800000, v44
	v_add_f32_e32 v42, 1.0, v42
	v_rcp_f32_e32 v42, v42
	s_nop 0
	v_mul_f32_e32 v42, v45, v42
	v_mul_f32_e32 v44, v42, v44
	v_max_f32_e32 v42, v79, v79
	v_min_f32_e32 v42, 0x44e00000, v42
	v_mul_f32_e32 v46, 0x37800000, v42
	v_mul_f32_e32 v42, 0xbc1d265f, v42
	v_exp_f32_e32 v42, v42
	v_med3_f32 v45, v173, s81, v139
	v_add_f32_e32 v45, 0x43800000, v45
	v_add_f32_e32 v42, 1.0, v42
	v_rcp_f32_e32 v42, v42
	s_nop 0
	v_mul_f32_e32 v42, v46, v42
	v_mul_f32_e32 v45, v42, v45
	v_max_f32_e32 v42, v75, v75
	v_min_f32_e32 v42, 0x44e00000, v42
	v_mul_f32_e32 v47, 0x37800000, v42
	v_mul_f32_e32 v42, 0xbc1d265f, v42
	v_exp_f32_e32 v42, v42
	v_med3_f32 v46, v19, s81, v139
	v_add_f32_e32 v46, 0x43800000, v46
	v_add_f32_e32 v42, 1.0, v42
	v_rcp_f32_e32 v42, v42
	s_nop 0
	v_mul_f32_e32 v42, v47, v42
	v_mul_f32_e32 v46, v42, v46
	v_max_f32_e32 v42, v80, v80
	v_min_f32_e32 v42, 0x44e00000, v42
	v_mul_f32_e32 v48, 0x37800000, v42
	v_mul_f32_e32 v42, 0xbc1d265f, v42
	v_exp_f32_e32 v42, v42
	v_med3_f32 v47, v174, s81, v139
	v_add_f32_e32 v47, 0x43800000, v47
	v_add_f32_e32 v42, 1.0, v42
	v_rcp_f32_e32 v42, v42
	s_nop 0
	v_mul_f32_e32 v42, v48, v42
	v_mul_f32_e32 v47, v42, v47
	v_max_f32_e32 v42, v76, v76
	v_min_f32_e32 v42, 0x44e00000, v42
	v_mul_f32_e32 v49, 0x37800000, v42
	v_mul_f32_e32 v42, 0xbc1d265f, v42
	v_exp_f32_e32 v42, v42
	v_med3_f32 v48, v20, s81, v139
	v_add_f32_e32 v48, 0x43800000, v48
	v_add_f32_e32 v42, 1.0, v42
	v_rcp_f32_e32 v42, v42
	s_nop 0
	v_mul_f32_e32 v42, v49, v42
	v_mul_f32_e32 v48, v42, v48
	v_max_f32_e32 v42, v81, v81
	v_min_f32_e32 v42, 0x44e00000, v42
	v_mul_f32_e32 v50, 0x37800000, v42
	v_mul_f32_e32 v42, 0xbc1d265f, v42
	v_exp_f32_e32 v42, v42
	v_med3_f32 v49, v175, s81, v139
	v_add_f32_e32 v49, 0x43800000, v49
	v_add_f32_e32 v42, 1.0, v42
	v_rcp_f32_e32 v42, v42
	s_nop 0
	v_mul_f32_e32 v42, v50, v42
	v_mul_f32_e32 v49, v42, v49
	v_max_f32_e32 v42, v77, v77
	v_min_f32_e32 v42, 0x44e00000, v42
	v_mul_f32_e32 v51, 0x37800000, v42
	v_mul_f32_e32 v42, 0xbc1d265f, v42
	v_exp_f32_e32 v42, v42
	v_med3_f32 v50, v21, s81, v139
	v_add_f32_e32 v50, 0x43800000, v50
	v_add_f32_e32 v42, 1.0, v42
	v_rcp_f32_e32 v42, v42
	s_nop 0
	v_mul_f32_e32 v42, v51, v42
	v_mul_f32_e32 v50, v42, v50
	v_mov_b32_e32 v42, v131
	v_cvt_pk_fp8_f32 v42, v43, v45
	v_mov_b32_e32 v43, v131
	v_cvt_pk_fp8_f32 v43, v44, v46
	v_lshl_add_u64 v[44:45], v[134:135], 0, s[34:35]
	v_cvt_pk_fp8_f32 v42, v47, v49 op_sel:[0,0,1]
	s_mov_b64 s[34:35], 0x18000
	v_cvt_pk_fp8_f32 v43, v48, v50 op_sel:[0,0,1]
	s_nop 0
	global_store_dwordx2 v[44:45], v[42:43], off sc1
	s_nop 1
	v_max_f32_e32 v42, v70, v70
	v_min_f32_e32 v42, 0x44e00000, v42
	v_mul_f32_e32 v44, 0x37800000, v42
	v_mul_f32_e32 v42, 0xbc1d265f, v42
	v_exp_f32_e32 v42, v42
	v_med3_f32 v43, v6, s81, v139
	v_add_f32_e32 v43, 0x43800000, v43
	v_add_f32_e32 v42, 1.0, v42
	v_rcp_f32_e32 v42, v42
	s_nop 0
	v_mul_f32_e32 v42, v44, v42
	v_mul_f32_e32 v43, v42, v43
	v_max_f32_e32 v42, v66, v66
	v_min_f32_e32 v42, 0x44e00000, v42
	v_mul_f32_e32 v45, 0x37800000, v42
	v_mul_f32_e32 v42, 0xbc1d265f, v42
	v_exp_f32_e32 v42, v42
	v_med3_f32 v44, v14, s81, v139
	v_add_f32_e32 v44, 0x43800000, v44
	v_add_f32_e32 v42, 1.0, v42
	v_rcp_f32_e32 v42, v42
	s_nop 0
	v_mul_f32_e32 v42, v45, v42
	v_mul_f32_e32 v44, v42, v44
	v_max_f32_e32 v42, v71, v71
	v_min_f32_e32 v42, 0x44e00000, v42
	v_mul_f32_e32 v46, 0x37800000, v42
	v_mul_f32_e32 v42, 0xbc1d265f, v42
	v_exp_f32_e32 v42, v42
	v_med3_f32 v45, v7, s81, v139
	v_add_f32_e32 v45, 0x43800000, v45
	v_add_f32_e32 v42, 1.0, v42
	v_rcp_f32_e32 v42, v42
	s_nop 0
	v_mul_f32_e32 v42, v46, v42
	v_mul_f32_e32 v45, v42, v45
	v_max_f32_e32 v42, v67, v67
	v_min_f32_e32 v42, 0x44e00000, v42
	v_mul_f32_e32 v47, 0x37800000, v42
	v_mul_f32_e32 v42, 0xbc1d265f, v42
	v_exp_f32_e32 v42, v42
	v_med3_f32 v46, v15, s81, v139
	v_add_f32_e32 v46, 0x43800000, v46
	v_add_f32_e32 v42, 1.0, v42
	v_rcp_f32_e32 v42, v42
	s_nop 0
	v_mul_f32_e32 v42, v47, v42
	v_mul_f32_e32 v46, v42, v46
	v_max_f32_e32 v42, v72, v72
	v_min_f32_e32 v42, 0x44e00000, v42
	v_mul_f32_e32 v48, 0x37800000, v42
	v_mul_f32_e32 v42, 0xbc1d265f, v42
	v_exp_f32_e32 v42, v42
	v_med3_f32 v47, v8, s81, v139
	v_add_f32_e32 v47, 0x43800000, v47
	v_add_f32_e32 v42, 1.0, v42
	v_rcp_f32_e32 v42, v42
	s_nop 0
	v_mul_f32_e32 v42, v48, v42
	v_mul_f32_e32 v47, v42, v47
	v_max_f32_e32 v42, v68, v68
	v_min_f32_e32 v42, 0x44e00000, v42
	v_mul_f32_e32 v49, 0x37800000, v42
	v_mul_f32_e32 v42, 0xbc1d265f, v42
	v_exp_f32_e32 v42, v42
	v_med3_f32 v48, v16, s81, v139
	v_add_f32_e32 v48, 0x43800000, v48
	v_add_f32_e32 v42, 1.0, v42
	v_rcp_f32_e32 v42, v42
	s_nop 0
	v_mul_f32_e32 v42, v49, v42
	v_mul_f32_e32 v48, v42, v48
	v_max_f32_e32 v42, v73, v73
	v_min_f32_e32 v42, 0x44e00000, v42
	v_mul_f32_e32 v50, 0x37800000, v42
	v_mul_f32_e32 v42, 0xbc1d265f, v42
	v_exp_f32_e32 v42, v42
	v_med3_f32 v49, v9, s81, v139
	v_add_f32_e32 v49, 0x43800000, v49
	v_add_f32_e32 v42, 1.0, v42
	v_rcp_f32_e32 v42, v42
	s_nop 0
	v_mul_f32_e32 v42, v50, v42
	v_mul_f32_e32 v49, v42, v49
	v_max_f32_e32 v42, v69, v69
	v_min_f32_e32 v42, 0x44e00000, v42
	v_mul_f32_e32 v51, 0x37800000, v42
	v_mul_f32_e32 v42, 0xbc1d265f, v42
	v_exp_f32_e32 v42, v42
	v_med3_f32 v50, v17, s81, v139
	v_add_f32_e32 v50, 0x43800000, v50
	v_add_f32_e32 v42, 1.0, v42
	v_rcp_f32_e32 v42, v42
	s_nop 0
	v_mul_f32_e32 v42, v51, v42
	v_mul_f32_e32 v50, v42, v50
	v_mov_b32_e32 v42, v131
	v_cvt_pk_fp8_f32 v42, v43, v45
	v_mov_b32_e32 v43, v131
	v_cvt_pk_fp8_f32 v43, v44, v46
	v_lshl_add_u64 v[44:45], v[134:135], 0, s[34:35]
	v_cvt_pk_fp8_f32 v42, v47, v49 op_sel:[0,0,1]
	s_mov_b64 s[34:35], 0x48000
	v_cvt_pk_fp8_f32 v43, v48, v50 op_sel:[0,0,1]
	s_nop 0
	global_store_dwordx2 v[44:45], v[42:43], off sc1
	s_nop 1
	v_max_f32_e32 v42, v38, v38
	v_min_f32_e32 v42, 0x44e00000, v42
	v_mul_f32_e32 v44, 0x37800000, v42
	v_mul_f32_e32 v42, 0xbc1d265f, v42
	v_exp_f32_e32 v42, v42
	v_med3_f32 v43, v98, s81, v139
	v_add_f32_e32 v43, 0x43800000, v43
	v_add_f32_e32 v42, 1.0, v42
	v_rcp_f32_e32 v42, v42
	s_nop 0
	v_mul_f32_e32 v42, v44, v42
	v_mul_f32_e32 v43, v42, v43
	v_max_f32_e32 v42, v34, v34
	v_min_f32_e32 v42, 0x44e00000, v42
	v_mul_f32_e32 v45, 0x37800000, v42
	v_mul_f32_e32 v42, 0xbc1d265f, v42
	v_exp_f32_e32 v42, v42
	v_med3_f32 v44, v102, s81, v139
	v_add_f32_e32 v44, 0x43800000, v44
	v_add_f32_e32 v42, 1.0, v42
	v_rcp_f32_e32 v42, v42
	s_nop 0
	v_mul_f32_e32 v42, v45, v42
	v_mul_f32_e32 v44, v42, v44
	v_max_f32_e32 v42, v39, v39
	v_min_f32_e32 v42, 0x44e00000, v42
	v_mul_f32_e32 v46, 0x37800000, v42
	v_mul_f32_e32 v42, 0xbc1d265f, v42
	v_exp_f32_e32 v42, v42
	v_med3_f32 v45, v99, s81, v139
	v_add_f32_e32 v45, 0x43800000, v45
	v_add_f32_e32 v42, 1.0, v42
	v_rcp_f32_e32 v42, v42
	s_nop 0
	v_mul_f32_e32 v42, v46, v42
	v_mul_f32_e32 v45, v42, v45
	v_max_f32_e32 v42, v35, v35
	v_min_f32_e32 v42, 0x44e00000, v42
	v_mul_f32_e32 v47, 0x37800000, v42
	v_mul_f32_e32 v42, 0xbc1d265f, v42
	v_exp_f32_e32 v42, v42
	v_med3_f32 v46, v103, s81, v139
	v_add_f32_e32 v46, 0x43800000, v46
	v_add_f32_e32 v42, 1.0, v42
	v_rcp_f32_e32 v42, v42
	s_nop 0
	v_mul_f32_e32 v42, v47, v42
	v_mul_f32_e32 v46, v42, v46
	v_max_f32_e32 v42, v40, v40
	v_min_f32_e32 v42, 0x44e00000, v42
	v_mul_f32_e32 v48, 0x37800000, v42
	v_mul_f32_e32 v42, 0xbc1d265f, v42
	v_exp_f32_e32 v42, v42
	v_med3_f32 v47, v100, s81, v139
	v_add_f32_e32 v47, 0x43800000, v47
	v_add_f32_e32 v42, 1.0, v42
	v_rcp_f32_e32 v42, v42
	s_nop 0
	v_mul_f32_e32 v42, v48, v42
	v_mul_f32_e32 v47, v42, v47
	v_max_f32_e32 v42, v36, v36
	v_min_f32_e32 v42, 0x44e00000, v42
	v_mul_f32_e32 v49, 0x37800000, v42
	v_mul_f32_e32 v42, 0xbc1d265f, v42
	v_exp_f32_e32 v42, v42
	v_med3_f32 v48, v104, s81, v139
	v_add_f32_e32 v48, 0x43800000, v48
	v_add_f32_e32 v42, 1.0, v42
	v_rcp_f32_e32 v42, v42
	s_nop 0
	v_mul_f32_e32 v42, v49, v42
	v_mul_f32_e32 v48, v42, v48
	v_max_f32_e32 v42, v41, v41
	v_min_f32_e32 v42, 0x44e00000, v42
	v_mul_f32_e32 v50, 0x37800000, v42
	v_mul_f32_e32 v42, 0xbc1d265f, v42
	v_exp_f32_e32 v42, v42
	v_med3_f32 v49, v101, s81, v139
	v_add_f32_e32 v49, 0x43800000, v49
	v_add_f32_e32 v42, 1.0, v42
	v_rcp_f32_e32 v42, v42
	s_nop 0
	v_mul_f32_e32 v42, v50, v42
	v_mul_f32_e32 v49, v42, v49
	v_max_f32_e32 v42, v37, v37
	v_min_f32_e32 v42, 0x44e00000, v42
	v_mul_f32_e32 v51, 0x37800000, v42
	v_mul_f32_e32 v42, 0xbc1d265f, v42
	v_exp_f32_e32 v42, v42
	v_med3_f32 v50, v105, s81, v139
	v_add_f32_e32 v50, 0x43800000, v50
	v_add_f32_e32 v42, 1.0, v42
	v_rcp_f32_e32 v42, v42
	s_nop 0
	v_mul_f32_e32 v42, v51, v42
	v_mul_f32_e32 v50, v42, v50
	v_mov_b32_e32 v42, v131
	v_cvt_pk_fp8_f32 v42, v43, v45
	v_mov_b32_e32 v43, v131
	v_cvt_pk_fp8_f32 v43, v44, v46
	v_lshl_add_u64 v[44:45], v[134:135], 0, s[18:19]
	v_cvt_pk_fp8_f32 v42, v47, v49 op_sel:[0,0,1]
	v_cvt_pk_fp8_f32 v43, v48, v50 op_sel:[0,0,1]
	s_nop 0
	global_store_dwordx2 v[44:45], v[42:43], off sc1
	s_nop 1
	v_max_f32_e32 v42, v30, v30
	v_min_f32_e32 v42, 0x44e00000, v42
	v_mul_f32_e32 v44, 0x37800000, v42
	v_mul_f32_e32 v42, 0xbc1d265f, v42
	v_exp_f32_e32 v42, v42
	v_med3_f32 v43, v106, s81, v139
	v_add_f32_e32 v43, 0x43800000, v43
	v_add_f32_e32 v42, 1.0, v42
	v_rcp_f32_e32 v42, v42
	s_nop 0
	v_mul_f32_e32 v42, v44, v42
	v_mul_f32_e32 v43, v42, v43
	v_max_f32_e32 v42, v26, v26
	v_min_f32_e32 v42, 0x44e00000, v42
	v_mul_f32_e32 v45, 0x37800000, v42
	v_mul_f32_e32 v42, 0xbc1d265f, v42
	v_exp_f32_e32 v42, v42
	v_med3_f32 v44, v110, s81, v139
	v_add_f32_e32 v44, 0x43800000, v44
	v_add_f32_e32 v42, 1.0, v42
	v_rcp_f32_e32 v42, v42
	s_nop 0
	v_mul_f32_e32 v42, v45, v42
	v_mul_f32_e32 v44, v42, v44
	v_max_f32_e32 v42, v31, v31
	v_min_f32_e32 v42, 0x44e00000, v42
	v_mul_f32_e32 v46, 0x37800000, v42
	v_mul_f32_e32 v42, 0xbc1d265f, v42
	v_exp_f32_e32 v42, v42
	v_med3_f32 v45, v107, s81, v139
	v_add_f32_e32 v45, 0x43800000, v45
	v_add_f32_e32 v42, 1.0, v42
	v_rcp_f32_e32 v42, v42
	s_nop 0
	v_mul_f32_e32 v42, v46, v42
	v_mul_f32_e32 v45, v42, v45
	v_max_f32_e32 v42, v27, v27
	v_min_f32_e32 v42, 0x44e00000, v42
	v_mul_f32_e32 v47, 0x37800000, v42
	v_mul_f32_e32 v42, 0xbc1d265f, v42
	v_exp_f32_e32 v42, v42
	v_med3_f32 v46, v111, s81, v139
	v_add_f32_e32 v46, 0x43800000, v46
	v_add_f32_e32 v42, 1.0, v42
	v_rcp_f32_e32 v42, v42
	s_nop 0
	v_mul_f32_e32 v42, v47, v42
	v_mul_f32_e32 v46, v42, v46
	v_max_f32_e32 v42, v32, v32
	v_min_f32_e32 v42, 0x44e00000, v42
	v_mul_f32_e32 v48, 0x37800000, v42
	v_mul_f32_e32 v42, 0xbc1d265f, v42
	v_exp_f32_e32 v42, v42
	v_med3_f32 v47, v108, s81, v139
	v_add_f32_e32 v47, 0x43800000, v47
	v_add_f32_e32 v42, 1.0, v42
	v_rcp_f32_e32 v42, v42
	s_nop 0
	v_mul_f32_e32 v42, v48, v42
	v_mul_f32_e32 v47, v42, v47
	v_max_f32_e32 v42, v28, v28
	v_min_f32_e32 v42, 0x44e00000, v42
	v_mul_f32_e32 v49, 0x37800000, v42
	v_mul_f32_e32 v42, 0xbc1d265f, v42
	v_exp_f32_e32 v42, v42
	v_med3_f32 v48, v112, s81, v139
	v_add_f32_e32 v48, 0x43800000, v48
	v_add_f32_e32 v42, 1.0, v42
	v_rcp_f32_e32 v42, v42
	s_nop 0
	v_mul_f32_e32 v42, v49, v42
	v_mul_f32_e32 v48, v42, v48
	v_max_f32_e32 v42, v33, v33
	v_min_f32_e32 v42, 0x44e00000, v42
	v_mul_f32_e32 v50, 0x37800000, v42
	v_mul_f32_e32 v42, 0xbc1d265f, v42
	v_exp_f32_e32 v42, v42
	v_med3_f32 v49, v109, s81, v139
	v_add_f32_e32 v49, 0x43800000, v49
	v_add_f32_e32 v42, 1.0, v42
	v_rcp_f32_e32 v42, v42
	s_nop 0
	v_mul_f32_e32 v42, v50, v42
	v_mul_f32_e32 v49, v42, v49
	v_max_f32_e32 v42, v29, v29
	v_min_f32_e32 v42, 0x44e00000, v42
	v_mul_f32_e32 v51, 0x37800000, v42
	v_mul_f32_e32 v42, 0xbc1d265f, v42
	v_exp_f32_e32 v42, v42
	v_med3_f32 v50, v113, s81, v139
	v_add_f32_e32 v50, 0x43800000, v50
	v_add_f32_e32 v42, 1.0, v42
	v_rcp_f32_e32 v42, v42
	s_nop 0
	v_mul_f32_e32 v42, v51, v42
	v_mul_f32_e32 v50, v42, v50
	v_mov_b32_e32 v42, v131
	v_cvt_pk_fp8_f32 v42, v43, v45
	v_mov_b32_e32 v43, v131
	v_cvt_pk_fp8_f32 v43, v44, v46
	v_lshl_add_u64 v[44:45], v[134:135], 0, s[34:35]
	v_cvt_pk_fp8_f32 v42, v47, v49 op_sel:[0,0,1]
	s_mov_b64 s[34:35], 0x50000
	v_cvt_pk_fp8_f32 v43, v48, v50 op_sel:[0,0,1]
	s_nop 0
	global_store_dwordx2 v[44:45], v[42:43], off sc1
	s_nop 1
	v_max_f32_e32 v42, v22, v22
	v_min_f32_e32 v42, 0x44e00000, v42
	v_mul_f32_e32 v44, 0x37800000, v42
	v_mul_f32_e32 v42, 0xbc1d265f, v42
	v_exp_f32_e32 v42, v42
	v_med3_f32 v43, v114, s81, v139
	v_add_f32_e32 v43, 0x43800000, v43
	v_add_f32_e32 v42, 1.0, v42
	v_rcp_f32_e32 v42, v42
	s_nop 0
	v_mul_f32_e32 v42, v44, v42
	v_mul_f32_e32 v43, v42, v43
	v_max_f32_e32 v42, v220, v220
	v_min_f32_e32 v42, 0x44e00000, v42
	v_mul_f32_e32 v45, 0x37800000, v42
	v_mul_f32_e32 v42, 0xbc1d265f, v42
	v_exp_f32_e32 v42, v42
	v_med3_f32 v44, v118, s81, v139
	v_add_f32_e32 v44, 0x43800000, v44
	v_add_f32_e32 v42, 1.0, v42
	v_rcp_f32_e32 v42, v42
	s_nop 0
	v_mul_f32_e32 v42, v45, v42
	v_mul_f32_e32 v44, v42, v44
	v_max_f32_e32 v42, v23, v23
	v_min_f32_e32 v42, 0x44e00000, v42
	v_mul_f32_e32 v46, 0x37800000, v42
	v_mul_f32_e32 v42, 0xbc1d265f, v42
	v_exp_f32_e32 v42, v42
	v_med3_f32 v45, v115, s81, v139
	v_add_f32_e32 v45, 0x43800000, v45
	v_add_f32_e32 v42, 1.0, v42
	v_rcp_f32_e32 v42, v42
	s_nop 0
	v_mul_f32_e32 v42, v46, v42
	v_mul_f32_e32 v45, v42, v45
	v_max_f32_e32 v42, v221, v221
	v_min_f32_e32 v42, 0x44e00000, v42
	v_mul_f32_e32 v47, 0x37800000, v42
	v_mul_f32_e32 v42, 0xbc1d265f, v42
	v_exp_f32_e32 v42, v42
	v_med3_f32 v46, v119, s81, v139
	v_add_f32_e32 v46, 0x43800000, v46
	v_add_f32_e32 v42, 1.0, v42
	v_rcp_f32_e32 v42, v42
	s_nop 0
	v_mul_f32_e32 v42, v47, v42
	v_mul_f32_e32 v46, v42, v46
	v_max_f32_e32 v42, v24, v24
	v_min_f32_e32 v42, 0x44e00000, v42
	v_mul_f32_e32 v48, 0x37800000, v42
	v_mul_f32_e32 v42, 0xbc1d265f, v42
	v_exp_f32_e32 v42, v42
	v_med3_f32 v47, v116, s81, v139
	v_add_f32_e32 v47, 0x43800000, v47
	v_add_f32_e32 v42, 1.0, v42
	v_rcp_f32_e32 v42, v42
	s_nop 0
	v_mul_f32_e32 v42, v48, v42
	v_mul_f32_e32 v47, v42, v47
	v_max_f32_e32 v42, v222, v222
	v_min_f32_e32 v42, 0x44e00000, v42
	v_mul_f32_e32 v49, 0x37800000, v42
	v_mul_f32_e32 v42, 0xbc1d265f, v42
	v_exp_f32_e32 v42, v42
	v_med3_f32 v48, v120, s81, v139
	v_add_f32_e32 v48, 0x43800000, v48
	v_add_f32_e32 v42, 1.0, v42
	v_rcp_f32_e32 v42, v42
	s_nop 0
	v_mul_f32_e32 v42, v49, v42
	v_mul_f32_e32 v48, v42, v48
	v_max_f32_e32 v42, v25, v25
	v_min_f32_e32 v42, 0x44e00000, v42
	v_mul_f32_e32 v50, 0x37800000, v42
	v_mul_f32_e32 v42, 0xbc1d265f, v42
	v_exp_f32_e32 v42, v42
	v_med3_f32 v49, v117, s81, v139
	v_add_f32_e32 v49, 0x43800000, v49
	v_add_f32_e32 v42, 1.0, v42
	v_rcp_f32_e32 v42, v42
	s_nop 0
	v_mul_f32_e32 v42, v50, v42
	v_mul_f32_e32 v49, v42, v49
	v_max_f32_e32 v42, v223, v223
	v_min_f32_e32 v42, 0x44e00000, v42
	v_mul_f32_e32 v51, 0x37800000, v42
	v_mul_f32_e32 v42, 0xbc1d265f, v42
	v_exp_f32_e32 v42, v42
	v_med3_f32 v50, v121, s81, v139
	v_add_f32_e32 v50, 0x43800000, v50
	v_add_f32_e32 v42, 1.0, v42
	v_rcp_f32_e32 v42, v42
	s_nop 0
	v_mul_f32_e32 v42, v51, v42
	v_mul_f32_e32 v50, v42, v50
	v_mov_b32_e32 v42, v131
	v_cvt_pk_fp8_f32 v42, v43, v45
	v_mov_b32_e32 v43, v131
	v_cvt_pk_fp8_f32 v43, v44, v46
	v_lshl_add_u64 v[44:45], v[134:135], 0, s[34:35]
	v_cvt_pk_fp8_f32 v42, v47, v49 op_sel:[0,0,1]
	s_mov_b64 s[34:35], 0x58000
	v_cvt_pk_fp8_f32 v43, v48, v50 op_sel:[0,0,1]
	s_nop 0
	global_store_dwordx2 v[44:45], v[42:43], off sc1
	s_nop 1
	v_max_f32_e32 v42, v2, v2
	v_min_f32_e32 v42, 0x44e00000, v42
	v_mul_f32_e32 v44, 0x37800000, v42
	v_mul_f32_e32 v42, 0xbc1d265f, v42
	v_exp_f32_e32 v42, v42
	v_med3_f32 v43, v122, s81, v139
	v_add_f32_e32 v43, 0x43800000, v43
	v_add_f32_e32 v42, 1.0, v42
	v_rcp_f32_e32 v42, v42
	s_nop 0
	v_mul_f32_e32 v42, v44, v42
	v_mul_f32_e32 v43, v42, v43
	v_max_f32_e32 v42, v10, v10
	v_min_f32_e32 v42, 0x44e00000, v42
	v_mul_f32_e32 v45, 0x37800000, v42
	v_mul_f32_e32 v42, 0xbc1d265f, v42
	v_exp_f32_e32 v42, v42
	v_med3_f32 v44, v126, s81, v139
	v_add_f32_e32 v44, 0x43800000, v44
	v_add_f32_e32 v42, 1.0, v42
	v_rcp_f32_e32 v42, v42
	s_nop 0
	v_mul_f32_e32 v42, v45, v42
	v_mul_f32_e32 v44, v42, v44
	v_max_f32_e32 v42, v3, v3
	v_min_f32_e32 v42, 0x44e00000, v42
	v_mul_f32_e32 v46, 0x37800000, v42
	v_mul_f32_e32 v42, 0xbc1d265f, v42
	v_exp_f32_e32 v42, v42
	v_med3_f32 v45, v123, s81, v139
	v_add_f32_e32 v45, 0x43800000, v45
	v_add_f32_e32 v42, 1.0, v42
	v_rcp_f32_e32 v42, v42
	s_nop 0
	v_mul_f32_e32 v42, v46, v42
	v_mul_f32_e32 v45, v42, v45
	v_max_f32_e32 v42, v11, v11
	v_min_f32_e32 v42, 0x44e00000, v42
	v_mul_f32_e32 v47, 0x37800000, v42
	v_mul_f32_e32 v42, 0xbc1d265f, v42
	v_exp_f32_e32 v42, v42
	v_med3_f32 v46, v127, s81, v139
	v_add_f32_e32 v46, 0x43800000, v46
	v_add_f32_e32 v42, 1.0, v42
	v_rcp_f32_e32 v42, v42
	s_nop 0
	v_mul_f32_e32 v42, v47, v42
	v_mul_f32_e32 v46, v42, v46
	v_max_f32_e32 v42, v4, v4
	v_min_f32_e32 v42, 0x44e00000, v42
	v_mul_f32_e32 v48, 0x37800000, v42
	v_mul_f32_e32 v42, 0xbc1d265f, v42
	v_exp_f32_e32 v42, v42
	v_med3_f32 v47, v124, s81, v139
	v_add_f32_e32 v47, 0x43800000, v47
	v_add_f32_e32 v42, 1.0, v42
	v_rcp_f32_e32 v42, v42
	s_nop 0
	v_mul_f32_e32 v42, v48, v42
	v_mul_f32_e32 v47, v42, v47
	v_max_f32_e32 v42, v12, v12
	v_min_f32_e32 v42, 0x44e00000, v42
	v_mul_f32_e32 v49, 0x37800000, v42
	v_mul_f32_e32 v42, 0xbc1d265f, v42
	v_exp_f32_e32 v42, v42
	v_med3_f32 v48, v128, s81, v139
	v_add_f32_e32 v48, 0x43800000, v48
	v_add_f32_e32 v42, 1.0, v42
	v_rcp_f32_e32 v42, v42
	s_nop 0
	v_mul_f32_e32 v42, v49, v42
	v_mul_f32_e32 v48, v42, v48
	v_max_f32_e32 v42, v5, v5
	v_min_f32_e32 v42, 0x44e00000, v42
	v_mul_f32_e32 v50, 0x37800000, v42
	v_mul_f32_e32 v42, 0xbc1d265f, v42
	v_exp_f32_e32 v42, v42
	v_med3_f32 v49, v125, s81, v139
	v_add_f32_e32 v49, 0x43800000, v49
	v_add_f32_e32 v42, 1.0, v42
	v_rcp_f32_e32 v42, v42
	s_nop 0
	v_mul_f32_e32 v42, v50, v42
	v_mul_f32_e32 v49, v42, v49
	v_max_f32_e32 v42, v13, v13
	v_min_f32_e32 v42, 0x44e00000, v42
	v_mul_f32_e32 v51, 0x37800000, v42
	v_mul_f32_e32 v42, 0xbc1d265f, v42
	v_exp_f32_e32 v42, v42
	v_med3_f32 v50, v129, s81, v139
	v_add_f32_e32 v50, 0x43800000, v50
	v_add_f32_e32 v42, 1.0, v42
	v_rcp_f32_e32 v42, v42
	s_nop 0
	v_mul_f32_e32 v42, v51, v42
	v_mul_f32_e32 v50, v42, v50
	v_mov_b32_e32 v42, v131
	v_cvt_pk_fp8_f32 v42, v43, v45
	v_mov_b32_e32 v43, v131
	v_cvt_pk_fp8_f32 v43, v44, v46
	v_lshl_add_u64 v[44:45], v[134:135], 0, s[34:35]
	v_cvt_pk_fp8_f32 v42, v47, v49 op_sel:[0,0,1]
	v_cvt_pk_fp8_f32 v43, v48, v50 op_sel:[0,0,1]
	s_nop 0
	global_store_dwordx2 v[44:45], v[42:43], off sc1
	s_nop 1
	s_cbranch_vccnz .LBB0_1269
	v_readlane_b32 s88, v254, 4
	s_ashr_i32 s45, s44, 31
	v_readlane_b32 s92, v254, 8
	v_readlane_b32 s93, v254, 9
	s_lshl_b64 s[4:5], s[44:45], 14
	s_mov_b64 s[56:57], s[92:93]
	s_add_u32 s22, s56, s4
	v_mov_b32_e32 v2, v131
	s_addc_u32 s34, s57, s5
	s_lshl_b32 s4, s46, 7
	s_ashr_i32 s5, s4, 31
	v_mbcnt_lo_u32_b32 v2, -1, v2
	s_lshl_b64 s[4:5], s[4:5], 2
	v_mbcnt_hi_u32_b32 v2, -1, v2
	s_add_u32 s4, s22, s4
	s_addc_u32 s5, s34, s5
	s_lshl_b32 s22, s63, 2
	v_ashrrev_i32_e32 v2, 1, v2
	s_add_u32 s4, s4, s22
	v_and_b32_e32 v2, -8, v2
	s_addc_u32 s5, s5, 0
	v_ashrrev_i32_e32 v3, 31, v2
	v_lshl_add_u64 v[6:7], v[2:3], 2, s[4:5]
	v_lshl_add_u64 v[14:15], v[6:7], 0, s[6:7]
	v_add_co_u32_e32 v6, vcc, 0x2000, v6
	v_readlane_b32 s89, v254, 5
	s_nop 0
	v_addc_co_u32_e32 v7, vcc, 0, v7, vcc
	s_nop 0
	s_andn2_b64 vcc, exec, s[24:25]
	v_readlane_b32 s90, v254, 6
	v_readlane_b32 s91, v254, 7
	v_readlane_b32 s94, v254, 10
	v_readlane_b32 s95, v254, 11
	s_cbranch_vccnz .LBB0_1268
	s_barrier
.LBB0_1268:
	s_waitcnt vmcnt(8)
	v_pk_mul_f32 v[4:5], v[142:143], s[38:39] op_sel_hi:[1,0]
	v_pk_mul_f32 v[8:9], v[146:147], s[38:39] op_sel_hi:[1,0]
	v_pk_mul_f32 v[12:13], v[150:151], s[38:39] op_sel_hi:[1,0]
	v_pk_mul_f32 v[16:17], v[154:155], s[38:39] op_sel_hi:[1,0]
	v_pk_mul_f32 v[2:3], v[140:141], s[38:39] op_sel_hi:[1,0]
	v_pk_mul_f32 v[6:7], v[144:145], s[38:39] op_sel_hi:[1,0]
	v_pk_mul_f32 v[10:11], v[148:149], s[38:39] op_sel_hi:[1,0]
	v_pk_mul_f32 v[14:15], v[152:153], s[38:39] op_sel_hi:[1,0]
	v_mov_b64_e32 v[222:223], v[12:13]
	v_mov_b64_e32 v[24:25], v[4:5]
	v_mov_b64_e32 v[28:29], v[12:13]
	v_mov_b64_e32 v[32:33], v[4:5]
	v_mov_b64_e32 v[36:37], v[12:13]
	v_mov_b64_e32 v[40:41], v[4:5]
	v_mov_b64_e32 v[20:21], v[16:17]
	v_mov_b64_e32 v[174:175], v[8:9]
	v_mov_b64_e32 v[178:179], v[16:17]
	v_mov_b64_e32 v[56:57], v[8:9]
	v_mov_b64_e32 v[60:61], v[16:17]
	v_mov_b64_e32 v[64:65], v[8:9]
	v_mov_b64_e32 v[68:69], v[12:13]
	v_mov_b64_e32 v[72:73], v[4:5]
	v_mov_b64_e32 v[76:77], v[12:13]
	v_mov_b64_e32 v[80:81], v[4:5]
	v_mov_b64_e32 v[84:85], v[12:13]
	v_mov_b64_e32 v[88:89], v[4:5]
	v_mov_b64_e32 v[92:93], v[12:13]
	v_mov_b64_e32 v[96:97], v[4:5]
	v_mov_b64_e32 v[100:101], v[8:9]
	v_mov_b64_e32 v[104:105], v[16:17]
	v_mov_b64_e32 v[108:109], v[8:9]
	v_mov_b64_e32 v[112:113], v[16:17]
	v_mov_b64_e32 v[116:117], v[8:9]
	v_mov_b64_e32 v[120:121], v[16:17]
	v_mov_b64_e32 v[124:125], v[8:9]
	v_mov_b64_e32 v[128:129], v[16:17]
	v_readlane_b32 s4, v255, 5
	v_mov_b64_e32 v[220:221], v[10:11]
	v_mov_b64_e32 v[22:23], v[2:3]
	v_mov_b64_e32 v[26:27], v[10:11]
	v_mov_b64_e32 v[30:31], v[2:3]
	v_mov_b64_e32 v[34:35], v[10:11]
	v_mov_b64_e32 v[38:39], v[2:3]
	v_mov_b64_e32 v[18:19], v[14:15]
	v_mov_b64_e32 v[172:173], v[6:7]
	v_mov_b64_e32 v[176:177], v[14:15]
	v_mov_b64_e32 v[54:55], v[6:7]
	v_mov_b64_e32 v[58:59], v[14:15]
	v_mov_b64_e32 v[62:63], v[6:7]
	v_mov_b64_e32 v[66:67], v[10:11]
	v_mov_b64_e32 v[70:71], v[2:3]
	v_mov_b64_e32 v[74:75], v[10:11]
	v_mov_b64_e32 v[78:79], v[2:3]
	v_mov_b64_e32 v[82:83], v[10:11]
	v_mov_b64_e32 v[86:87], v[2:3]
	v_mov_b64_e32 v[90:91], v[10:11]
	v_mov_b64_e32 v[94:95], v[2:3]
	v_mov_b64_e32 v[98:99], v[6:7]
	v_mov_b64_e32 v[102:103], v[14:15]
	v_mov_b64_e32 v[106:107], v[6:7]
	v_mov_b64_e32 v[110:111], v[14:15]
	v_mov_b64_e32 v[114:115], v[6:7]
	v_mov_b64_e32 v[118:119], v[14:15]
	v_mov_b64_e32 v[122:123], v[6:7]
	v_mov_b64_e32 v[126:127], v[14:15]
	s_mov_b32 s45, s44
	s_mov_b32 s22, s46
	s_mov_b32 s47, s84
	s_mov_b32 s74, s64
	s_mov_b32 s83, s65
	s_mov_b32 s80, s4
	v_readlane_b32 s5, v255, 6
	s_andn2_b64 vcc, exec, s[48:49]
	s_cbranch_vccnz .LBB0_1270
	s_branch .LBB0_1271
